# hand-written scanner (D=20 ring, counted vmcnt) + hand-written gatherer fast path (DPP reductions, batched LDS reads, 64-entry single pass)
# speedup vs baseline: 1.0066x; 1.0066x over previous
_Z11attn_kernelPKfS0_PKDv8_DF16_S0_Pfi:
	v_cmp_gt_u32_e32 vcc, 8, v0
	s_and_saveexec_b64 s[4:5], vcc
	v_lshlrev_b32_e32 v1, 2, v0
	v_mov_b32_e32 v2, 0
	ds_write_b32 v1, v2 offset:36864
	s_or_b64 exec, exec, s[4:5]
	s_load_dword s33, s[0:1], 0x28
	v_bfe_u32 v1, v0, 6, 2
	v_lshl_or_b32 v82, s2, 2, v1
	s_waitcnt lgkmcnt(0)
	s_barrier
	v_cmp_gt_i32_e32 vcc, s33, v82
	s_and_saveexec_b64 s[4:5], vcc
	s_cbranch_execz .LBB1_384
	s_abs_i32 s3, s33
	v_cvt_f32_u32_e32 v2, s3
	s_movk_i32 s4, 0xff
	v_sub_u32_e32 v3, 0x270f, v82
	v_cmp_lt_u32_e32 vcc, s4, v0
	v_rcp_iflag_f32_e32 v2, v2
	v_sub_u32_e32 v5, 0, v3
	s_sub_i32 s4, 0, s3
	v_xor_b32_e32 v4, s33, v3
	v_mul_f32_e32 v2, 0x4f7ffffe, v2
	v_cvt_u32_f32_e32 v2, v2
	v_max_i32_e32 v3, v3, v5
	s_load_dwordx2 s[28:29], s[0:1], 0x0
	v_ashrrev_i32_e32 v4, 31, v4
	v_mul_lo_u32 v5, s4, v2
	v_mul_hi_u32 v5, v2, v5
	v_add_u32_e32 v2, v2, v5
	v_mul_hi_u32 v2, v3, v2
	v_mul_lo_u32 v5, v2, s3
	v_sub_u32_e32 v3, v3, v5
	v_add_u32_e32 v5, 1, v2
	v_cmp_le_u32_e64 s[4:5], s3, v3
	v_and_b32_e32 v83, 63, v0
	s_nop 0
	v_cndmask_b32_e64 v2, v2, v5, s[4:5]
	v_subrev_u32_e32 v5, s3, v3
	v_cndmask_b32_e64 v3, v3, v5, s[4:5]
	v_add_u32_e32 v5, 1, v2
	v_cmp_le_u32_e64 s[4:5], s3, v3
	s_nop 1
	v_cndmask_b32_e64 v2, v2, v5, s[4:5]
	v_xor_b32_e32 v2, v2, v4
	v_sub_u32_e32 v84, v2, v4
	s_and_saveexec_b64 s[4:5], vcc
	s_xor_b64 s[30:31], exec, s[4:5]
	s_cbranch_execz .LBB1_217
	v_cmp_lt_i32_e32 vcc, -1, v84
	s_and_saveexec_b64 s[34:35], vcc
	s_cbranch_execz .LBB1_216
	s_load_dwordx8 s[20:27], s[0:1], 0x8
	v_and_b32_e32 v69, 15, v0
	v_mov_b32_e32 v0, 0x8000
	v_lshrrev_b32_e32 v67, 4, v83
	v_lshl_or_b32 v88, v1, 10, v0
	s_mul_i32 s3, s2, 0x2710
	v_mul_u32_u24_e32 v0, 0x9c4, v1
	v_lshl_or_b32 v89, v69, 2, v67
	v_add3_u32 v90, s3, v0, v83
	v_lshlrev_b32_e32 v0, 2, v1
	v_mov_b32_e32 v2, 0x9000
	v_lshl_or_b32 v91, s2, 4, v0
	v_lshlrev_b32_e32 v0, 3, v89
	v_mov_b32_e32 v32, 0
	v_lshl_or_b32 v65, v1, 3, v2
	v_or_b32_e32 v2, 0x1e00, v0
	v_mov_b32_e32 v3, v32
	s_waitcnt lgkmcnt(0)
	v_lshl_add_u64 v[34:35], s[20:21], 0, v[2:3]
	v_or_b32_e32 v2, 0x1c00, v0
	v_lshl_add_u64 v[36:37], s[20:21], 0, v[2:3]
	v_or_b32_e32 v2, 0x1a00, v0
	v_lshl_add_u64 v[38:39], s[20:21], 0, v[2:3]
	v_or_b32_e32 v2, 0x1800, v0
	v_lshl_add_u64 v[40:41], s[20:21], 0, v[2:3]
	v_or_b32_e32 v2, 0x1600, v0
	v_lshl_add_u64 v[42:43], s[20:21], 0, v[2:3]
	v_or_b32_e32 v2, 0x1400, v0
	v_lshlrev_b32_e32 v63, 12, v1
	v_lshl_add_u64 v[44:45], s[20:21], 0, v[2:3]
	v_or_b32_e32 v2, 0x1200, v0
	v_mov_b32_e32 v1, v32
	v_lshl_or_b32 v71, v83, 3, v63
	v_lshl_or_b32 v73, v67, 3, v63
	v_lshl_add_u64 v[46:47], s[20:21], 0, v[2:3]
	v_or_b32_e32 v2, 0x1000, v0
	v_lshl_add_u64 v[50:51], s[20:21], 0, v[0:1]
	v_mbcnt_lo_u32_b32 v0, -1, 0
	v_or_b32_e32 v75, 4, v67
	v_or_b32_e32 v77, 8, v67
	v_or_b32_e32 v78, 12, v67
	v_or_b32_e32 v79, 16, v67
	v_or_b32_e32 v80, 20, v67
	v_or_b32_e32 v81, 24, v67
	v_or_b32_e32 v85, 28, v67
	v_or_b32_e32 v86, 64, v83
	v_or_b32_e32 v87, 0x4000, v63
	v_cmp_lt_u32_e64 s[0:1], 15, v83
	s_mul_i32 s39, s33, 0x9c4
	s_lshl_b32 s48, s33, 2
	v_or_b32_e32 v92, 0x200, v71
	v_or_b32_e32 v93, 0x204, v71
	v_or_b32_e32 v94, 0x100, v73
	v_lshl_add_u64 v[48:49], s[20:21], 0, v[2:3]
	s_mov_b32 s51, 0
	s_mov_b64 s[36:37], 0
	s_movk_i32 s49, 0x81
	s_mov_b32 s50, 0xff800000
	s_mov_b32 s38, 0x38d1b717
	v_mov_b32_e32 v95, 0xff800000
	v_mbcnt_hi_u32_b32 v96, -1, v0
	v_mov_b32_e32 v136, 0
	v_mov_b32_e32 v137, 0
	v_mov_b32_e32 v138, 0
	v_mov_b32_e32 v139, 0
	v_mov_b32_e32 v140, 0
	v_mov_b32_e32 v141, 0
	v_mov_b32_e32 v142, 0
	v_mov_b32_e32 v143, 0
	v_mov_b32_e32 v144, 0
	v_mov_b32_e32 v145, 0
	v_mov_b32_e32 v146, 0
	v_mov_b32_e32 v147, 0
	v_mov_b32_e32 v148, 0
	v_mov_b32_e32 v149, 0
	v_mov_b32_e32 v150, 0
	v_mov_b32_e32 v151, 0
	v_mov_b32_e32 v152, 0
	v_mov_b32_e32 v153, 0
	v_mov_b32_e32 v154, 0
	v_mov_b32_e32 v155, 0
	v_mov_b32_e32 v156, 0
	v_mov_b32_e32 v157, 0
	v_mov_b32_e32 v158, 0
	v_mov_b32_e32 v159, 0
	v_mov_b32_e32 v160, 0
	v_mov_b32_e32 v161, 0
	v_mov_b32_e32 v162, 0
	v_mov_b32_e32 v163, 0
	v_mov_b32_e32 v164, 0
	v_mov_b32_e32 v165, 0
	v_mov_b32_e32 v166, 0
	v_mov_b32_e32 v167, 0
	v_mov_b32_e32 v168, 0
	v_mov_b32_e32 v169, 0
	v_mov_b32_e32 v170, 0
	v_mov_b32_e32 v171, 0
	v_mov_b32_e32 v172, 0
	v_mov_b32_e32 v173, 0
	v_mov_b32_e32 v174, 0
	v_mov_b32_e32 v175, 0
	v_mov_b32_e32 v176, 0
	v_mov_b32_e32 v177, 0
	v_mov_b32_e32 v178, 0
	v_mov_b32_e32 v179, 0
	v_mov_b32_e32 v180, 0
	v_mov_b32_e32 v181, 0
	v_mov_b32_e32 v182, 0
	v_mov_b32_e32 v183, 0
	v_mov_b32_e32 v184, 0
	v_mov_b32_e32 v185, 0
	v_mov_b32_e32 v186, 0
	v_mov_b32_e32 v187, 0
	v_mov_b32_e32 v188, 0
	v_mov_b32_e32 v189, 0
	v_mov_b32_e32 v190, 0
	v_mov_b32_e32 v191, 0
	v_mov_b32_e32 v192, 0
	v_mov_b32_e32 v193, 0
	v_mov_b32_e32 v194, 0
	v_mov_b32_e32 v195, 0
	v_mov_b32_e32 v196, 0
	v_mov_b32_e32 v197, 0
	v_mov_b32_e32 v198, 0
	v_mov_b32_e32 v199, 0
	s_branch .LBB1_9

.LBB1_13:
	s_or_b64 exec, exec, s[2:3]
	s_mul_i32 s2, s51, s33
	v_add_u32_e32 v97, s2, v82
	v_readfirstlane_b32 s4, v0
	s_sub_i32 s4, s4, 1
	s_cmp_gt_u32 s4, 64
	s_cbranch_scc1 .Lg_slow
	s_lshl_b32 s5, s46, 11
	v_lshl_add_u32 v1, v83, 4, v87
	v_add_u32_e32 v1, s5, v1
	s_lshl_b32 s5, s46, 9
	v_lshl_add_u32 v2, v83, 2, v88
	v_add_u32_e32 v2, s5, v2
	ds_read_b128 v[8:11], v1
	ds_read_b32 v12, v2
	v_cmp_gt_u32_e64 s[6:7], s4, v83
	v_lshlrev_b32_e32 v25, 4, v69
	s_waitcnt lgkmcnt(0)
	v_cmp_neq_f32_e32 vcc, 0, v8
	s_and_b64 s[8:9], vcc, s[6:7]
	v_cmp_neq_f32_e32 vcc, 0, v9
	s_and_b64 s[10:11], vcc, s[6:7]
	v_cmp_neq_f32_e32 vcc, 0, v10
	s_and_b64 s[12:13], vcc, s[6:7]
	v_cmp_neq_f32_e32 vcc, 0, v11
	s_and_b64 s[14:15], vcc, s[6:7]
	s_bcnt1_i32_b64 s16, s[8:9]
	s_bcnt1_i32_b64 s17, s[10:11]
	s_bcnt1_i32_b64 s18, s[12:13]
	s_bcnt1_i32_b64 s19, s[14:15]
	s_add_i32 s17, s17, s16
	s_add_i32 s18, s18, s17
	s_add_i32 s19, s19, s18
	s_cmp_eq_u32 s19, 0
	s_cbranch_scc1 .Lg_slow
	s_cmp_gt_u32 s19, 64
	s_cbranch_scc1 .Lg_slow
	v_mbcnt_lo_u32_b32 v13, s8, 0
	v_mbcnt_hi_u32_b32 v13, s9, v13
	v_lshl_add_u32 v14, v13, 3, v63
	v_mov_b32_e32 v4, v12
	v_mov_b32_e32 v5, v8
	s_mov_b64 exec, s[8:9]
	ds_write_b64 v14, v[4:5]
	s_mov_b64 exec, -1
	v_mbcnt_lo_u32_b32 v13, s10, 0
	v_mbcnt_hi_u32_b32 v13, s11, v13
	v_add_u32_e32 v13, s16, v13
	v_lshl_add_u32 v14, v13, 3, v63
	v_add_u32_e32 v4, 1, v12
	v_mov_b32_e32 v5, v9
	s_mov_b64 exec, s[10:11]
	ds_write_b64 v14, v[4:5]
	s_mov_b64 exec, -1
	v_mbcnt_lo_u32_b32 v13, s12, 0
	v_mbcnt_hi_u32_b32 v13, s13, v13
	v_add_u32_e32 v13, s17, v13
	v_lshl_add_u32 v14, v13, 3, v63
	v_add_u32_e32 v4, 2, v12
	v_mov_b32_e32 v5, v10
	s_mov_b64 exec, s[12:13]
	ds_write_b64 v14, v[4:5]
	s_mov_b64 exec, -1
	v_mbcnt_lo_u32_b32 v13, s14, 0
	v_mbcnt_hi_u32_b32 v13, s15, v13
	v_add_u32_e32 v13, s18, v13
	v_lshl_add_u32 v14, v13, 3, v63
	v_add_u32_e32 v4, 3, v12
	v_mov_b32_e32 v5, v11
	s_mov_b64 exec, s[14:15]
	ds_write_b64 v14, v[4:5]
	s_mov_b64 exec, -1
	v_mov_b32_e32 v4, 0
	ds_write_b32 v6, v4
	v_lshl_add_u32 v14, v83, 3, v63
	ds_read_b64 v[16:17], v14
	v_lshl_add_u32 v22, v67, 3, v63
	ds_read_b32 v116, v22
	ds_read_b32 v117, v22 offset:32
	ds_read_b32 v118, v22 offset:64
	ds_read_b32 v119, v22 offset:96
	ds_read_b32 v120, v22 offset:128
	ds_read_b32 v121, v22 offset:160
	ds_read_b32 v122, v22 offset:192
	ds_read_b32 v123, v22 offset:224
	v_sub_u32_e32 v23, s19, v67
	v_cmp_gt_u32_e64 s[6:7], s19, v83
	s_waitcnt lgkmcnt(8)
	v_cndmask_b32_e64 v15, 0, v16, s[6:7]
	v_lshlrev_b32_e32 v15, 2, v15
	global_load_dword v18, v15, s[24:25]
	s_cmp_gt_u32 s19, 32
	s_cbranch_scc1 .Lg_big
	s_waitcnt lgkmcnt(0)
	v_cmp_lt_i32_e32 vcc, 0, v23
	v_lshl_add_u32 v24, v116, 8, v25
	s_mov_b64 exec, vcc
	global_load_dwordx4 v[136:139], v24, s[22:23]
	s_mov_b64 exec, -1
	v_cmp_lt_i32_e32 vcc, 4, v23
	v_lshl_add_u32 v24, v117, 8, v25
	s_mov_b64 exec, vcc
	global_load_dwordx4 v[140:143], v24, s[22:23]
	s_mov_b64 exec, -1
	v_cmp_lt_i32_e32 vcc, 8, v23
	v_lshl_add_u32 v24, v118, 8, v25
	s_mov_b64 exec, vcc
	global_load_dwordx4 v[144:147], v24, s[22:23]
	s_mov_b64 exec, -1
	v_cmp_lt_i32_e32 vcc, 12, v23
	v_lshl_add_u32 v24, v119, 8, v25
	s_mov_b64 exec, vcc
	global_load_dwordx4 v[148:151], v24, s[22:23]
	s_mov_b64 exec, -1
	v_cmp_lt_i32_e32 vcc, 16, v23
	v_lshl_add_u32 v24, v120, 8, v25
	s_mov_b64 exec, vcc
	global_load_dwordx4 v[152:155], v24, s[22:23]
	s_mov_b64 exec, -1
	v_cmp_lt_i32_e32 vcc, 20, v23
	v_lshl_add_u32 v24, v121, 8, v25
	s_mov_b64 exec, vcc
	global_load_dwordx4 v[156:159], v24, s[22:23]
	s_mov_b64 exec, -1
	v_cmp_lt_i32_e32 vcc, 24, v23
	v_lshl_add_u32 v24, v122, 8, v25
	s_mov_b64 exec, vcc
	global_load_dwordx4 v[160:163], v24, s[22:23]
	s_mov_b64 exec, -1
	v_cmp_lt_i32_e32 vcc, 28, v23
	v_lshl_add_u32 v24, v123, 8, v25
	s_mov_b64 exec, vcc
	global_load_dwordx4 v[164:167], v24, s[22:23]
	s_mov_b64 exec, -1
	s_waitcnt vmcnt(8)
	s_branch .Lg_soft
.Lg_big:
	ds_read_b32 v124, v22 offset:256
	ds_read_b32 v125, v22 offset:288
	ds_read_b32 v126, v22 offset:320
	ds_read_b32 v127, v22 offset:352
	ds_read_b32 v128, v22 offset:384
	ds_read_b32 v129, v22 offset:416
	ds_read_b32 v130, v22 offset:448
	ds_read_b32 v131, v22 offset:480
	s_waitcnt lgkmcnt(8)
	v_cmp_lt_i32_e32 vcc, 0, v23
	v_lshl_add_u32 v24, v116, 8, v25
	s_mov_b64 exec, vcc
	global_load_dwordx4 v[136:139], v24, s[22:23]
	s_mov_b64 exec, -1
	v_cmp_lt_i32_e32 vcc, 4, v23
	v_lshl_add_u32 v24, v117, 8, v25
	s_mov_b64 exec, vcc
	global_load_dwordx4 v[140:143], v24, s[22:23]
	s_mov_b64 exec, -1
	v_cmp_lt_i32_e32 vcc, 8, v23
	v_lshl_add_u32 v24, v118, 8, v25
	s_mov_b64 exec, vcc
	global_load_dwordx4 v[144:147], v24, s[22:23]
	s_mov_b64 exec, -1
	v_cmp_lt_i32_e32 vcc, 12, v23
	v_lshl_add_u32 v24, v119, 8, v25
	s_mov_b64 exec, vcc
	global_load_dwordx4 v[148:151], v24, s[22:23]
	s_mov_b64 exec, -1
	v_cmp_lt_i32_e32 vcc, 16, v23
	v_lshl_add_u32 v24, v120, 8, v25
	s_mov_b64 exec, vcc
	global_load_dwordx4 v[152:155], v24, s[22:23]
	s_mov_b64 exec, -1
	v_cmp_lt_i32_e32 vcc, 20, v23
	v_lshl_add_u32 v24, v121, 8, v25
	s_mov_b64 exec, vcc
	global_load_dwordx4 v[156:159], v24, s[22:23]
	s_mov_b64 exec, -1
	v_cmp_lt_i32_e32 vcc, 24, v23
	v_lshl_add_u32 v24, v122, 8, v25
	s_mov_b64 exec, vcc
	global_load_dwordx4 v[160:163], v24, s[22:23]
	s_mov_b64 exec, -1
	v_cmp_lt_i32_e32 vcc, 28, v23
	v_lshl_add_u32 v24, v123, 8, v25
	s_mov_b64 exec, vcc
	global_load_dwordx4 v[164:167], v24, s[22:23]
	s_mov_b64 exec, -1
	s_waitcnt lgkmcnt(0)
	v_cmp_lt_i32_e32 vcc, 32, v23
	v_lshl_add_u32 v24, v124, 8, v25
	s_mov_b64 exec, vcc
	global_load_dwordx4 v[168:171], v24, s[22:23]
	s_mov_b64 exec, -1
	v_cmp_lt_i32_e32 vcc, 36, v23
	v_lshl_add_u32 v24, v125, 8, v25
	s_mov_b64 exec, vcc
	global_load_dwordx4 v[172:175], v24, s[22:23]
	s_mov_b64 exec, -1
	v_cmp_lt_i32_e32 vcc, 40, v23
	v_lshl_add_u32 v24, v126, 8, v25
	s_mov_b64 exec, vcc
	global_load_dwordx4 v[176:179], v24, s[22:23]
	s_mov_b64 exec, -1
	v_cmp_lt_i32_e32 vcc, 44, v23
	v_lshl_add_u32 v24, v127, 8, v25
	s_mov_b64 exec, vcc
	global_load_dwordx4 v[180:183], v24, s[22:23]
	s_mov_b64 exec, -1
	v_cmp_lt_i32_e32 vcc, 48, v23
	v_lshl_add_u32 v24, v128, 8, v25
	s_mov_b64 exec, vcc
	global_load_dwordx4 v[184:187], v24, s[22:23]
	s_mov_b64 exec, -1
	v_cmp_lt_i32_e32 vcc, 52, v23
	v_lshl_add_u32 v24, v129, 8, v25
	s_mov_b64 exec, vcc
	global_load_dwordx4 v[188:191], v24, s[22:23]
	s_mov_b64 exec, -1
	v_cmp_lt_i32_e32 vcc, 56, v23
	v_lshl_add_u32 v24, v130, 8, v25
	s_mov_b64 exec, vcc
	global_load_dwordx4 v[192:195], v24, s[22:23]
	s_mov_b64 exec, -1
	v_cmp_lt_i32_e32 vcc, 60, v23
	v_lshl_add_u32 v24, v131, 8, v25
	s_mov_b64 exec, vcc
	global_load_dwordx4 v[196:199], v24, s[22:23]
	s_mov_b64 exec, -1
	s_waitcnt vmcnt(16)
.Lg_soft:
	v_mul_f32_e32 v18, v17, v18
	v_cndmask_b32_e64 v18, v95, v18, s[6:7]
	s_nop 1
	v_max_f32_dpp v20, v18, v18 quad_perm:[1,0,3,2] row_mask:0xf bank_mask:0xf
	s_nop 1
	v_max_f32_dpp v20, v20, v20 quad_perm:[2,3,0,1] row_mask:0xf bank_mask:0xf
	s_nop 1
	v_max_f32_dpp v20, v20, v20 row_half_mirror row_mask:0xf bank_mask:0xf
	s_nop 1
	v_max_f32_dpp v20, v20, v20 row_mirror row_mask:0xf bank_mask:0xf
	s_nop 1
	v_max_f32_dpp v20, v20, v20 row_bcast:15 row_mask:0xa bank_mask:0xf
	s_nop 1
	v_max_f32_dpp v20, v20, v20 row_bcast:31 row_mask:0xc bank_mask:0xf
	s_nop 1
	v_readlane_b32 s52, v20, 63
	s_nop 1
	v_subrev_f32_e32 v19, s52, v18
	v_mul_f32_e32 v19, 0x3fb8aa3b, v19
	v_exp_f32_e32 v19, v19
	s_nop 1
	ds_write_b32 v14, v19 offset:4
	ds_read_b32 v200, v22 offset:4
	ds_read_b32 v202, v22 offset:36
	ds_read_b32 v204, v22 offset:68
	ds_read_b32 v206, v22 offset:100
	ds_read_b32 v208, v22 offset:132
	ds_read_b32 v210, v22 offset:164
	ds_read_b32 v212, v22 offset:196
	ds_read_b32 v214, v22 offset:228
	v_add_f32_dpp v21, v19, v19 quad_perm:[1,0,3,2] row_mask:0xf bank_mask:0xf
	s_nop 1
	v_add_f32_dpp v21, v21, v21 quad_perm:[2,3,0,1] row_mask:0xf bank_mask:0xf
	s_nop 1
	v_add_f32_dpp v21, v21, v21 row_half_mirror row_mask:0xf bank_mask:0xf
	s_nop 1
	v_add_f32_dpp v21, v21, v21 row_mirror row_mask:0xf bank_mask:0xf
	s_nop 1
	v_add_f32_dpp v21, v21, v21 row_bcast:15 row_mask:0xa bank_mask:0xf
	s_nop 1
	v_add_f32_dpp v21, v21, v21 row_bcast:31 row_mask:0xc bank_mask:0xf
	s_nop 1
	v_readlane_b32 s53, v21, 63
	s_nop 1
	v_mov_b32_e32 v232, 0
	v_mov_b32_e32 v233, 0
	v_mov_b32_e32 v234, 0
	v_mov_b32_e32 v235, 0
	v_mov_b32_e32 v236, 0
	v_mov_b32_e32 v237, 0
	v_mov_b32_e32 v238, 0
	v_mov_b32_e32 v239, 0
	s_cmp_gt_u32 s19, 32
	s_cbranch_scc1 .Lg_acc_big
	s_waitcnt vmcnt(0) lgkmcnt(0)
	v_cvt_f32_f16_e32 v240, v136
	v_cvt_f32_f16_sdwa v241, v136 dst_sel:DWORD dst_unused:UNUSED_PAD src0_sel:WORD_1
	v_cvt_f32_f16_e32 v242, v137
	v_cvt_f32_f16_sdwa v243, v137 dst_sel:DWORD dst_unused:UNUSED_PAD src0_sel:WORD_1
	v_cvt_f32_f16_e32 v244, v138
	v_cvt_f32_f16_sdwa v245, v138 dst_sel:DWORD dst_unused:UNUSED_PAD src0_sel:WORD_1
	v_cvt_f32_f16_e32 v246, v139
	v_cvt_f32_f16_sdwa v247, v139 dst_sel:DWORD dst_unused:UNUSED_PAD src0_sel:WORD_1
	v_pk_fma_f32 v[232:233], v[200:201], v[240:241], v[232:233] op_sel_hi:[0,1,1]
	v_pk_fma_f32 v[234:235], v[200:201], v[242:243], v[234:235] op_sel_hi:[0,1,1]
	v_pk_fma_f32 v[236:237], v[200:201], v[244:245], v[236:237] op_sel_hi:[0,1,1]
	v_pk_fma_f32 v[238:239], v[200:201], v[246:247], v[238:239] op_sel_hi:[0,1,1]
	v_cvt_f32_f16_e32 v240, v140
	v_cvt_f32_f16_sdwa v241, v140 dst_sel:DWORD dst_unused:UNUSED_PAD src0_sel:WORD_1
	v_cvt_f32_f16_e32 v242, v141
	v_cvt_f32_f16_sdwa v243, v141 dst_sel:DWORD dst_unused:UNUSED_PAD src0_sel:WORD_1
	v_cvt_f32_f16_e32 v244, v142
	v_cvt_f32_f16_sdwa v245, v142 dst_sel:DWORD dst_unused:UNUSED_PAD src0_sel:WORD_1
	v_cvt_f32_f16_e32 v246, v143
	v_cvt_f32_f16_sdwa v247, v143 dst_sel:DWORD dst_unused:UNUSED_PAD src0_sel:WORD_1
	v_pk_fma_f32 v[232:233], v[202:203], v[240:241], v[232:233] op_sel_hi:[0,1,1]
	v_pk_fma_f32 v[234:235], v[202:203], v[242:243], v[234:235] op_sel_hi:[0,1,1]
	v_pk_fma_f32 v[236:237], v[202:203], v[244:245], v[236:237] op_sel_hi:[0,1,1]
	v_pk_fma_f32 v[238:239], v[202:203], v[246:247], v[238:239] op_sel_hi:[0,1,1]
	v_cvt_f32_f16_e32 v240, v144
	v_cvt_f32_f16_sdwa v241, v144 dst_sel:DWORD dst_unused:UNUSED_PAD src0_sel:WORD_1
	v_cvt_f32_f16_e32 v242, v145
	v_cvt_f32_f16_sdwa v243, v145 dst_sel:DWORD dst_unused:UNUSED_PAD src0_sel:WORD_1
	v_cvt_f32_f16_e32 v244, v146
	v_cvt_f32_f16_sdwa v245, v146 dst_sel:DWORD dst_unused:UNUSED_PAD src0_sel:WORD_1
	v_cvt_f32_f16_e32 v246, v147
	v_cvt_f32_f16_sdwa v247, v147 dst_sel:DWORD dst_unused:UNUSED_PAD src0_sel:WORD_1
	v_pk_fma_f32 v[232:233], v[204:205], v[240:241], v[232:233] op_sel_hi:[0,1,1]
	v_pk_fma_f32 v[234:235], v[204:205], v[242:243], v[234:235] op_sel_hi:[0,1,1]
	v_pk_fma_f32 v[236:237], v[204:205], v[244:245], v[236:237] op_sel_hi:[0,1,1]
	v_pk_fma_f32 v[238:239], v[204:205], v[246:247], v[238:239] op_sel_hi:[0,1,1]
	v_cvt_f32_f16_e32 v240, v148
	v_cvt_f32_f16_sdwa v241, v148 dst_sel:DWORD dst_unused:UNUSED_PAD src0_sel:WORD_1
	v_cvt_f32_f16_e32 v242, v149
	v_cvt_f32_f16_sdwa v243, v149 dst_sel:DWORD dst_unused:UNUSED_PAD src0_sel:WORD_1
	v_cvt_f32_f16_e32 v244, v150
	v_cvt_f32_f16_sdwa v245, v150 dst_sel:DWORD dst_unused:UNUSED_PAD src0_sel:WORD_1
	v_cvt_f32_f16_e32 v246, v151
	v_cvt_f32_f16_sdwa v247, v151 dst_sel:DWORD dst_unused:UNUSED_PAD src0_sel:WORD_1
	v_pk_fma_f32 v[232:233], v[206:207], v[240:241], v[232:233] op_sel_hi:[0,1,1]
	v_pk_fma_f32 v[234:235], v[206:207], v[242:243], v[234:235] op_sel_hi:[0,1,1]
	v_pk_fma_f32 v[236:237], v[206:207], v[244:245], v[236:237] op_sel_hi:[0,1,1]
	v_pk_fma_f32 v[238:239], v[206:207], v[246:247], v[238:239] op_sel_hi:[0,1,1]
	v_cvt_f32_f16_e32 v240, v152
	v_cvt_f32_f16_sdwa v241, v152 dst_sel:DWORD dst_unused:UNUSED_PAD src0_sel:WORD_1
	v_cvt_f32_f16_e32 v242, v153
	v_cvt_f32_f16_sdwa v243, v153 dst_sel:DWORD dst_unused:UNUSED_PAD src0_sel:WORD_1
	v_cvt_f32_f16_e32 v244, v154
	v_cvt_f32_f16_sdwa v245, v154 dst_sel:DWORD dst_unused:UNUSED_PAD src0_sel:WORD_1
	v_cvt_f32_f16_e32 v246, v155
	v_cvt_f32_f16_sdwa v247, v155 dst_sel:DWORD dst_unused:UNUSED_PAD src0_sel:WORD_1
	v_pk_fma_f32 v[232:233], v[208:209], v[240:241], v[232:233] op_sel_hi:[0,1,1]
	v_pk_fma_f32 v[234:235], v[208:209], v[242:243], v[234:235] op_sel_hi:[0,1,1]
	v_pk_fma_f32 v[236:237], v[208:209], v[244:245], v[236:237] op_sel_hi:[0,1,1]
	v_pk_fma_f32 v[238:239], v[208:209], v[246:247], v[238:239] op_sel_hi:[0,1,1]
	v_cvt_f32_f16_e32 v240, v156
	v_cvt_f32_f16_sdwa v241, v156 dst_sel:DWORD dst_unused:UNUSED_PAD src0_sel:WORD_1
	v_cvt_f32_f16_e32 v242, v157
	v_cvt_f32_f16_sdwa v243, v157 dst_sel:DWORD dst_unused:UNUSED_PAD src0_sel:WORD_1
	v_cvt_f32_f16_e32 v244, v158
	v_cvt_f32_f16_sdwa v245, v158 dst_sel:DWORD dst_unused:UNUSED_PAD src0_sel:WORD_1
	v_cvt_f32_f16_e32 v246, v159
	v_cvt_f32_f16_sdwa v247, v159 dst_sel:DWORD dst_unused:UNUSED_PAD src0_sel:WORD_1
	v_pk_fma_f32 v[232:233], v[210:211], v[240:241], v[232:233] op_sel_hi:[0,1,1]
	v_pk_fma_f32 v[234:235], v[210:211], v[242:243], v[234:235] op_sel_hi:[0,1,1]
	v_pk_fma_f32 v[236:237], v[210:211], v[244:245], v[236:237] op_sel_hi:[0,1,1]
	v_pk_fma_f32 v[238:239], v[210:211], v[246:247], v[238:239] op_sel_hi:[0,1,1]
	v_cvt_f32_f16_e32 v240, v160
	v_cvt_f32_f16_sdwa v241, v160 dst_sel:DWORD dst_unused:UNUSED_PAD src0_sel:WORD_1
	v_cvt_f32_f16_e32 v242, v161
	v_cvt_f32_f16_sdwa v243, v161 dst_sel:DWORD dst_unused:UNUSED_PAD src0_sel:WORD_1
	v_cvt_f32_f16_e32 v244, v162
	v_cvt_f32_f16_sdwa v245, v162 dst_sel:DWORD dst_unused:UNUSED_PAD src0_sel:WORD_1
	v_cvt_f32_f16_e32 v246, v163
	v_cvt_f32_f16_sdwa v247, v163 dst_sel:DWORD dst_unused:UNUSED_PAD src0_sel:WORD_1
	v_pk_fma_f32 v[232:233], v[212:213], v[240:241], v[232:233] op_sel_hi:[0,1,1]
	v_pk_fma_f32 v[234:235], v[212:213], v[242:243], v[234:235] op_sel_hi:[0,1,1]
	v_pk_fma_f32 v[236:237], v[212:213], v[244:245], v[236:237] op_sel_hi:[0,1,1]
	v_pk_fma_f32 v[238:239], v[212:213], v[246:247], v[238:239] op_sel_hi:[0,1,1]
	v_cvt_f32_f16_e32 v240, v164
	v_cvt_f32_f16_sdwa v241, v164 dst_sel:DWORD dst_unused:UNUSED_PAD src0_sel:WORD_1
	v_cvt_f32_f16_e32 v242, v165
	v_cvt_f32_f16_sdwa v243, v165 dst_sel:DWORD dst_unused:UNUSED_PAD src0_sel:WORD_1
	v_cvt_f32_f16_e32 v244, v166
	v_cvt_f32_f16_sdwa v245, v166 dst_sel:DWORD dst_unused:UNUSED_PAD src0_sel:WORD_1
	v_cvt_f32_f16_e32 v246, v167
	v_cvt_f32_f16_sdwa v247, v167 dst_sel:DWORD dst_unused:UNUSED_PAD src0_sel:WORD_1
	v_pk_fma_f32 v[232:233], v[214:215], v[240:241], v[232:233] op_sel_hi:[0,1,1]
	v_pk_fma_f32 v[234:235], v[214:215], v[242:243], v[234:235] op_sel_hi:[0,1,1]
	v_pk_fma_f32 v[236:237], v[214:215], v[244:245], v[236:237] op_sel_hi:[0,1,1]
	v_pk_fma_f32 v[238:239], v[214:215], v[246:247], v[238:239] op_sel_hi:[0,1,1]
	s_branch .Lg_fin
.Lg_acc_big:
	ds_read_b32 v216, v22 offset:260
	ds_read_b32 v218, v22 offset:292
	ds_read_b32 v220, v22 offset:324
	ds_read_b32 v222, v22 offset:356
	ds_read_b32 v224, v22 offset:388
	ds_read_b32 v226, v22 offset:420
	ds_read_b32 v228, v22 offset:452
	ds_read_b32 v230, v22 offset:484
	s_waitcnt vmcnt(0) lgkmcnt(0)
	v_cvt_f32_f16_e32 v240, v136
	v_cvt_f32_f16_sdwa v241, v136 dst_sel:DWORD dst_unused:UNUSED_PAD src0_sel:WORD_1
	v_cvt_f32_f16_e32 v242, v137
	v_cvt_f32_f16_sdwa v243, v137 dst_sel:DWORD dst_unused:UNUSED_PAD src0_sel:WORD_1
	v_cvt_f32_f16_e32 v244, v138
	v_cvt_f32_f16_sdwa v245, v138 dst_sel:DWORD dst_unused:UNUSED_PAD src0_sel:WORD_1
	v_cvt_f32_f16_e32 v246, v139
	v_cvt_f32_f16_sdwa v247, v139 dst_sel:DWORD dst_unused:UNUSED_PAD src0_sel:WORD_1
	v_pk_fma_f32 v[232:233], v[200:201], v[240:241], v[232:233] op_sel_hi:[0,1,1]
	v_pk_fma_f32 v[234:235], v[200:201], v[242:243], v[234:235] op_sel_hi:[0,1,1]
	v_pk_fma_f32 v[236:237], v[200:201], v[244:245], v[236:237] op_sel_hi:[0,1,1]
	v_pk_fma_f32 v[238:239], v[200:201], v[246:247], v[238:239] op_sel_hi:[0,1,1]
	v_cvt_f32_f16_e32 v240, v140
	v_cvt_f32_f16_sdwa v241, v140 dst_sel:DWORD dst_unused:UNUSED_PAD src0_sel:WORD_1
	v_cvt_f32_f16_e32 v242, v141
	v_cvt_f32_f16_sdwa v243, v141 dst_sel:DWORD dst_unused:UNUSED_PAD src0_sel:WORD_1
	v_cvt_f32_f16_e32 v244, v142
	v_cvt_f32_f16_sdwa v245, v142 dst_sel:DWORD dst_unused:UNUSED_PAD src0_sel:WORD_1
	v_cvt_f32_f16_e32 v246, v143
	v_cvt_f32_f16_sdwa v247, v143 dst_sel:DWORD dst_unused:UNUSED_PAD src0_sel:WORD_1
	v_pk_fma_f32 v[232:233], v[202:203], v[240:241], v[232:233] op_sel_hi:[0,1,1]
	v_pk_fma_f32 v[234:235], v[202:203], v[242:243], v[234:235] op_sel_hi:[0,1,1]
	v_pk_fma_f32 v[236:237], v[202:203], v[244:245], v[236:237] op_sel_hi:[0,1,1]
	v_pk_fma_f32 v[238:239], v[202:203], v[246:247], v[238:239] op_sel_hi:[0,1,1]
	v_cvt_f32_f16_e32 v240, v144
	v_cvt_f32_f16_sdwa v241, v144 dst_sel:DWORD dst_unused:UNUSED_PAD src0_sel:WORD_1
	v_cvt_f32_f16_e32 v242, v145
	v_cvt_f32_f16_sdwa v243, v145 dst_sel:DWORD dst_unused:UNUSED_PAD src0_sel:WORD_1
	v_cvt_f32_f16_e32 v244, v146
	v_cvt_f32_f16_sdwa v245, v146 dst_sel:DWORD dst_unused:UNUSED_PAD src0_sel:WORD_1
	v_cvt_f32_f16_e32 v246, v147
	v_cvt_f32_f16_sdwa v247, v147 dst_sel:DWORD dst_unused:UNUSED_PAD src0_sel:WORD_1
	v_pk_fma_f32 v[232:233], v[204:205], v[240:241], v[232:233] op_sel_hi:[0,1,1]
	v_pk_fma_f32 v[234:235], v[204:205], v[242:243], v[234:235] op_sel_hi:[0,1,1]
	v_pk_fma_f32 v[236:237], v[204:205], v[244:245], v[236:237] op_sel_hi:[0,1,1]
	v_pk_fma_f32 v[238:239], v[204:205], v[246:247], v[238:239] op_sel_hi:[0,1,1]
	v_cvt_f32_f16_e32 v240, v148
	v_cvt_f32_f16_sdwa v241, v148 dst_sel:DWORD dst_unused:UNUSED_PAD src0_sel:WORD_1
	v_cvt_f32_f16_e32 v242, v149
	v_cvt_f32_f16_sdwa v243, v149 dst_sel:DWORD dst_unused:UNUSED_PAD src0_sel:WORD_1
	v_cvt_f32_f16_e32 v244, v150
	v_cvt_f32_f16_sdwa v245, v150 dst_sel:DWORD dst_unused:UNUSED_PAD src0_sel:WORD_1
	v_cvt_f32_f16_e32 v246, v151
	v_cvt_f32_f16_sdwa v247, v151 dst_sel:DWORD dst_unused:UNUSED_PAD src0_sel:WORD_1
	v_pk_fma_f32 v[232:233], v[206:207], v[240:241], v[232:233] op_sel_hi:[0,1,1]
	v_pk_fma_f32 v[234:235], v[206:207], v[242:243], v[234:235] op_sel_hi:[0,1,1]
	v_pk_fma_f32 v[236:237], v[206:207], v[244:245], v[236:237] op_sel_hi:[0,1,1]
	v_pk_fma_f32 v[238:239], v[206:207], v[246:247], v[238:239] op_sel_hi:[0,1,1]
	v_cvt_f32_f16_e32 v240, v152
	v_cvt_f32_f16_sdwa v241, v152 dst_sel:DWORD dst_unused:UNUSED_PAD src0_sel:WORD_1
	v_cvt_f32_f16_e32 v242, v153
	v_cvt_f32_f16_sdwa v243, v153 dst_sel:DWORD dst_unused:UNUSED_PAD src0_sel:WORD_1
	v_cvt_f32_f16_e32 v244, v154
	v_cvt_f32_f16_sdwa v245, v154 dst_sel:DWORD dst_unused:UNUSED_PAD src0_sel:WORD_1
	v_cvt_f32_f16_e32 v246, v155
	v_cvt_f32_f16_sdwa v247, v155 dst_sel:DWORD dst_unused:UNUSED_PAD src0_sel:WORD_1
	v_pk_fma_f32 v[232:233], v[208:209], v[240:241], v[232:233] op_sel_hi:[0,1,1]
	v_pk_fma_f32 v[234:235], v[208:209], v[242:243], v[234:235] op_sel_hi:[0,1,1]
	v_pk_fma_f32 v[236:237], v[208:209], v[244:245], v[236:237] op_sel_hi:[0,1,1]
	v_pk_fma_f32 v[238:239], v[208:209], v[246:247], v[238:239] op_sel_hi:[0,1,1]
	v_cvt_f32_f16_e32 v240, v156
	v_cvt_f32_f16_sdwa v241, v156 dst_sel:DWORD dst_unused:UNUSED_PAD src0_sel:WORD_1
	v_cvt_f32_f16_e32 v242, v157
	v_cvt_f32_f16_sdwa v243, v157 dst_sel:DWORD dst_unused:UNUSED_PAD src0_sel:WORD_1
	v_cvt_f32_f16_e32 v244, v158
	v_cvt_f32_f16_sdwa v245, v158 dst_sel:DWORD dst_unused:UNUSED_PAD src0_sel:WORD_1
	v_cvt_f32_f16_e32 v246, v159
	v_cvt_f32_f16_sdwa v247, v159 dst_sel:DWORD dst_unused:UNUSED_PAD src0_sel:WORD_1
	v_pk_fma_f32 v[232:233], v[210:211], v[240:241], v[232:233] op_sel_hi:[0,1,1]
	v_pk_fma_f32 v[234:235], v[210:211], v[242:243], v[234:235] op_sel_hi:[0,1,1]
	v_pk_fma_f32 v[236:237], v[210:211], v[244:245], v[236:237] op_sel_hi:[0,1,1]
	v_pk_fma_f32 v[238:239], v[210:211], v[246:247], v[238:239] op_sel_hi:[0,1,1]
	v_cvt_f32_f16_e32 v240, v160
	v_cvt_f32_f16_sdwa v241, v160 dst_sel:DWORD dst_unused:UNUSED_PAD src0_sel:WORD_1
	v_cvt_f32_f16_e32 v242, v161
	v_cvt_f32_f16_sdwa v243, v161 dst_sel:DWORD dst_unused:UNUSED_PAD src0_sel:WORD_1
	v_cvt_f32_f16_e32 v244, v162
	v_cvt_f32_f16_sdwa v245, v162 dst_sel:DWORD dst_unused:UNUSED_PAD src0_sel:WORD_1
	v_cvt_f32_f16_e32 v246, v163
	v_cvt_f32_f16_sdwa v247, v163 dst_sel:DWORD dst_unused:UNUSED_PAD src0_sel:WORD_1
	v_pk_fma_f32 v[232:233], v[212:213], v[240:241], v[232:233] op_sel_hi:[0,1,1]
	v_pk_fma_f32 v[234:235], v[212:213], v[242:243], v[234:235] op_sel_hi:[0,1,1]
	v_pk_fma_f32 v[236:237], v[212:213], v[244:245], v[236:237] op_sel_hi:[0,1,1]
	v_pk_fma_f32 v[238:239], v[212:213], v[246:247], v[238:239] op_sel_hi:[0,1,1]
	v_cvt_f32_f16_e32 v240, v164
	v_cvt_f32_f16_sdwa v241, v164 dst_sel:DWORD dst_unused:UNUSED_PAD src0_sel:WORD_1
	v_cvt_f32_f16_e32 v242, v165
	v_cvt_f32_f16_sdwa v243, v165 dst_sel:DWORD dst_unused:UNUSED_PAD src0_sel:WORD_1
	v_cvt_f32_f16_e32 v244, v166
	v_cvt_f32_f16_sdwa v245, v166 dst_sel:DWORD dst_unused:UNUSED_PAD src0_sel:WORD_1
	v_cvt_f32_f16_e32 v246, v167
	v_cvt_f32_f16_sdwa v247, v167 dst_sel:DWORD dst_unused:UNUSED_PAD src0_sel:WORD_1
	v_pk_fma_f32 v[232:233], v[214:215], v[240:241], v[232:233] op_sel_hi:[0,1,1]
	v_pk_fma_f32 v[234:235], v[214:215], v[242:243], v[234:235] op_sel_hi:[0,1,1]
	v_pk_fma_f32 v[236:237], v[214:215], v[244:245], v[236:237] op_sel_hi:[0,1,1]
	v_pk_fma_f32 v[238:239], v[214:215], v[246:247], v[238:239] op_sel_hi:[0,1,1]
	v_cvt_f32_f16_e32 v240, v168
	v_cvt_f32_f16_sdwa v241, v168 dst_sel:DWORD dst_unused:UNUSED_PAD src0_sel:WORD_1
	v_cvt_f32_f16_e32 v242, v169
	v_cvt_f32_f16_sdwa v243, v169 dst_sel:DWORD dst_unused:UNUSED_PAD src0_sel:WORD_1
	v_cvt_f32_f16_e32 v244, v170
	v_cvt_f32_f16_sdwa v245, v170 dst_sel:DWORD dst_unused:UNUSED_PAD src0_sel:WORD_1
	v_cvt_f32_f16_e32 v246, v171
	v_cvt_f32_f16_sdwa v247, v171 dst_sel:DWORD dst_unused:UNUSED_PAD src0_sel:WORD_1
	v_pk_fma_f32 v[232:233], v[216:217], v[240:241], v[232:233] op_sel_hi:[0,1,1]
	v_pk_fma_f32 v[234:235], v[216:217], v[242:243], v[234:235] op_sel_hi:[0,1,1]
	v_pk_fma_f32 v[236:237], v[216:217], v[244:245], v[236:237] op_sel_hi:[0,1,1]
	v_pk_fma_f32 v[238:239], v[216:217], v[246:247], v[238:239] op_sel_hi:[0,1,1]
	v_cvt_f32_f16_e32 v240, v172
	v_cvt_f32_f16_sdwa v241, v172 dst_sel:DWORD dst_unused:UNUSED_PAD src0_sel:WORD_1
	v_cvt_f32_f16_e32 v242, v173
	v_cvt_f32_f16_sdwa v243, v173 dst_sel:DWORD dst_unused:UNUSED_PAD src0_sel:WORD_1
	v_cvt_f32_f16_e32 v244, v174
	v_cvt_f32_f16_sdwa v245, v174 dst_sel:DWORD dst_unused:UNUSED_PAD src0_sel:WORD_1
	v_cvt_f32_f16_e32 v246, v175
	v_cvt_f32_f16_sdwa v247, v175 dst_sel:DWORD dst_unused:UNUSED_PAD src0_sel:WORD_1
	v_pk_fma_f32 v[232:233], v[218:219], v[240:241], v[232:233] op_sel_hi:[0,1,1]
	v_pk_fma_f32 v[234:235], v[218:219], v[242:243], v[234:235] op_sel_hi:[0,1,1]
	v_pk_fma_f32 v[236:237], v[218:219], v[244:245], v[236:237] op_sel_hi:[0,1,1]
	v_pk_fma_f32 v[238:239], v[218:219], v[246:247], v[238:239] op_sel_hi:[0,1,1]
	v_cvt_f32_f16_e32 v240, v176
	v_cvt_f32_f16_sdwa v241, v176 dst_sel:DWORD dst_unused:UNUSED_PAD src0_sel:WORD_1
	v_cvt_f32_f16_e32 v242, v177
	v_cvt_f32_f16_sdwa v243, v177 dst_sel:DWORD dst_unused:UNUSED_PAD src0_sel:WORD_1
	v_cvt_f32_f16_e32 v244, v178
	v_cvt_f32_f16_sdwa v245, v178 dst_sel:DWORD dst_unused:UNUSED_PAD src0_sel:WORD_1
	v_cvt_f32_f16_e32 v246, v179
	v_cvt_f32_f16_sdwa v247, v179 dst_sel:DWORD dst_unused:UNUSED_PAD src0_sel:WORD_1
	v_pk_fma_f32 v[232:233], v[220:221], v[240:241], v[232:233] op_sel_hi:[0,1,1]
	v_pk_fma_f32 v[234:235], v[220:221], v[242:243], v[234:235] op_sel_hi:[0,1,1]
	v_pk_fma_f32 v[236:237], v[220:221], v[244:245], v[236:237] op_sel_hi:[0,1,1]
	v_pk_fma_f32 v[238:239], v[220:221], v[246:247], v[238:239] op_sel_hi:[0,1,1]
	v_cvt_f32_f16_e32 v240, v180
	v_cvt_f32_f16_sdwa v241, v180 dst_sel:DWORD dst_unused:UNUSED_PAD src0_sel:WORD_1
	v_cvt_f32_f16_e32 v242, v181
	v_cvt_f32_f16_sdwa v243, v181 dst_sel:DWORD dst_unused:UNUSED_PAD src0_sel:WORD_1
	v_cvt_f32_f16_e32 v244, v182
	v_cvt_f32_f16_sdwa v245, v182 dst_sel:DWORD dst_unused:UNUSED_PAD src0_sel:WORD_1
	v_cvt_f32_f16_e32 v246, v183
	v_cvt_f32_f16_sdwa v247, v183 dst_sel:DWORD dst_unused:UNUSED_PAD src0_sel:WORD_1
	v_pk_fma_f32 v[232:233], v[222:223], v[240:241], v[232:233] op_sel_hi:[0,1,1]
	v_pk_fma_f32 v[234:235], v[222:223], v[242:243], v[234:235] op_sel_hi:[0,1,1]
	v_pk_fma_f32 v[236:237], v[222:223], v[244:245], v[236:237] op_sel_hi:[0,1,1]
	v_pk_fma_f32 v[238:239], v[222:223], v[246:247], v[238:239] op_sel_hi:[0,1,1]
	v_cvt_f32_f16_e32 v240, v184
	v_cvt_f32_f16_sdwa v241, v184 dst_sel:DWORD dst_unused:UNUSED_PAD src0_sel:WORD_1
	v_cvt_f32_f16_e32 v242, v185
	v_cvt_f32_f16_sdwa v243, v185 dst_sel:DWORD dst_unused:UNUSED_PAD src0_sel:WORD_1
	v_cvt_f32_f16_e32 v244, v186
	v_cvt_f32_f16_sdwa v245, v186 dst_sel:DWORD dst_unused:UNUSED_PAD src0_sel:WORD_1
	v_cvt_f32_f16_e32 v246, v187
	v_cvt_f32_f16_sdwa v247, v187 dst_sel:DWORD dst_unused:UNUSED_PAD src0_sel:WORD_1
	v_pk_fma_f32 v[232:233], v[224:225], v[240:241], v[232:233] op_sel_hi:[0,1,1]
	v_pk_fma_f32 v[234:235], v[224:225], v[242:243], v[234:235] op_sel_hi:[0,1,1]
	v_pk_fma_f32 v[236:237], v[224:225], v[244:245], v[236:237] op_sel_hi:[0,1,1]
	v_pk_fma_f32 v[238:239], v[224:225], v[246:247], v[238:239] op_sel_hi:[0,1,1]
	v_cvt_f32_f16_e32 v240, v188
	v_cvt_f32_f16_sdwa v241, v188 dst_sel:DWORD dst_unused:UNUSED_PAD src0_sel:WORD_1
	v_cvt_f32_f16_e32 v242, v189
	v_cvt_f32_f16_sdwa v243, v189 dst_sel:DWORD dst_unused:UNUSED_PAD src0_sel:WORD_1
	v_cvt_f32_f16_e32 v244, v190
	v_cvt_f32_f16_sdwa v245, v190 dst_sel:DWORD dst_unused:UNUSED_PAD src0_sel:WORD_1
	v_cvt_f32_f16_e32 v246, v191
	v_cvt_f32_f16_sdwa v247, v191 dst_sel:DWORD dst_unused:UNUSED_PAD src0_sel:WORD_1
	v_pk_fma_f32 v[232:233], v[226:227], v[240:241], v[232:233] op_sel_hi:[0,1,1]
	v_pk_fma_f32 v[234:235], v[226:227], v[242:243], v[234:235] op_sel_hi:[0,1,1]
	v_pk_fma_f32 v[236:237], v[226:227], v[244:245], v[236:237] op_sel_hi:[0,1,1]
	v_pk_fma_f32 v[238:239], v[226:227], v[246:247], v[238:239] op_sel_hi:[0,1,1]
	v_cvt_f32_f16_e32 v240, v192
	v_cvt_f32_f16_sdwa v241, v192 dst_sel:DWORD dst_unused:UNUSED_PAD src0_sel:WORD_1
	v_cvt_f32_f16_e32 v242, v193
	v_cvt_f32_f16_sdwa v243, v193 dst_sel:DWORD dst_unused:UNUSED_PAD src0_sel:WORD_1
	v_cvt_f32_f16_e32 v244, v194
	v_cvt_f32_f16_sdwa v245, v194 dst_sel:DWORD dst_unused:UNUSED_PAD src0_sel:WORD_1
	v_cvt_f32_f16_e32 v246, v195
	v_cvt_f32_f16_sdwa v247, v195 dst_sel:DWORD dst_unused:UNUSED_PAD src0_sel:WORD_1
	v_pk_fma_f32 v[232:233], v[228:229], v[240:241], v[232:233] op_sel_hi:[0,1,1]
	v_pk_fma_f32 v[234:235], v[228:229], v[242:243], v[234:235] op_sel_hi:[0,1,1]
	v_pk_fma_f32 v[236:237], v[228:229], v[244:245], v[236:237] op_sel_hi:[0,1,1]
	v_pk_fma_f32 v[238:239], v[228:229], v[246:247], v[238:239] op_sel_hi:[0,1,1]
	v_cvt_f32_f16_e32 v240, v196
	v_cvt_f32_f16_sdwa v241, v196 dst_sel:DWORD dst_unused:UNUSED_PAD src0_sel:WORD_1
	v_cvt_f32_f16_e32 v242, v197
	v_cvt_f32_f16_sdwa v243, v197 dst_sel:DWORD dst_unused:UNUSED_PAD src0_sel:WORD_1
	v_cvt_f32_f16_e32 v244, v198
	v_cvt_f32_f16_sdwa v245, v198 dst_sel:DWORD dst_unused:UNUSED_PAD src0_sel:WORD_1
	v_cvt_f32_f16_e32 v246, v199
	v_cvt_f32_f16_sdwa v247, v199 dst_sel:DWORD dst_unused:UNUSED_PAD src0_sel:WORD_1
	v_pk_fma_f32 v[232:233], v[230:231], v[240:241], v[232:233] op_sel_hi:[0,1,1]
	v_pk_fma_f32 v[234:235], v[230:231], v[242:243], v[234:235] op_sel_hi:[0,1,1]
	v_pk_fma_f32 v[236:237], v[230:231], v[244:245], v[236:237] op_sel_hi:[0,1,1]
	v_pk_fma_f32 v[238:239], v[230:231], v[246:247], v[238:239] op_sel_hi:[0,1,1]
.Lg_fin:
	v_mov_b32_e32 v240, v232
	v_mov_b32_e32 v241, v233
	v_mov_b32_e32 v242, v234
	v_mov_b32_e32 v243, v235
	v_mov_b32_e32 v244, v236
	v_mov_b32_e32 v245, v237
	v_mov_b32_e32 v246, v238
	v_mov_b32_e32 v247, v239
	s_nop 1
	v_permlane32_swap_b32 v232, v240
	v_permlane32_swap_b32 v233, v241
	v_permlane32_swap_b32 v234, v242
	v_permlane32_swap_b32 v235, v243
	v_permlane32_swap_b32 v236, v244
	v_permlane32_swap_b32 v237, v245
	v_permlane32_swap_b32 v238, v246
	v_permlane32_swap_b32 v239, v247
	s_nop 1
	v_add_f32_e32 v232, v232, v240
	v_add_f32_e32 v233, v233, v241
	v_add_f32_e32 v234, v234, v242
	v_add_f32_e32 v235, v235, v243
	v_add_f32_e32 v236, v236, v244
	v_add_f32_e32 v237, v237, v245
	v_add_f32_e32 v238, v238, v246
	v_add_f32_e32 v239, v239, v247
	v_mov_b32_e32 v240, v232
	v_mov_b32_e32 v241, v233
	v_mov_b32_e32 v242, v234
	v_mov_b32_e32 v243, v235
	v_mov_b32_e32 v244, v236
	v_mov_b32_e32 v245, v237
	v_mov_b32_e32 v246, v238
	v_mov_b32_e32 v247, v239
	s_nop 1
	v_permlane16_swap_b32 v232, v240
	v_permlane16_swap_b32 v233, v241
	v_permlane16_swap_b32 v234, v242
	v_permlane16_swap_b32 v235, v243
	v_permlane16_swap_b32 v236, v244
	v_permlane16_swap_b32 v237, v245
	v_permlane16_swap_b32 v238, v246
	v_permlane16_swap_b32 v239, v247
	s_nop 1
	v_add_f32_e32 v232, v232, v240
	v_add_f32_e32 v233, v233, v241
	v_add_f32_e32 v234, v234, v242
	v_add_f32_e32 v235, v235, v243
	v_add_f32_e32 v236, v236, v244
	v_add_f32_e32 v237, v237, v245
	v_add_f32_e32 v238, v238, v246
	v_add_f32_e32 v239, v239, v247
	v_mov_b32_e32 v26, s53
	v_div_scale_f32 v27, s[2:3], v26, v26, 1.0
	v_rcp_f32_e32 v28, v27
	v_div_scale_f32 v29, vcc, 1.0, v26, 1.0
	v_fma_f32 v30, -v27, v28, 1.0
	v_fmac_f32_e32 v28, v30, v28
	v_mul_f32_e32 v30, v29, v28
	v_fma_f32 v31, -v27, v30, v29
	v_fmac_f32_e32 v30, v31, v28
	v_fma_f32 v27, -v27, v30, v29
	v_div_fmas_f32 v27, v27, v28, v30
	v_div_fixup_f32 v27, v27, v26, 1.0
	s_mov_b32 s8, 0xffff
	s_mov_b32 s9, 0
	s_mov_b32 s10, 0xffff0000
	s_mov_b32 s11, 0
	s_mov_b32 s12, 0
	s_mov_b32 s13, 0xffff
	v_cndmask_b32_e64 v0, v238, v236, s[12:13]
	v_cndmask_b32_e64 v0, v0, v234, s[10:11]
	v_cndmask_b32_e64 v0, v0, v232, s[8:9]
	v_cndmask_b32_e64 v1, v239, v237, s[12:13]
	v_cndmask_b32_e64 v1, v1, v235, s[10:11]
	v_cndmask_b32_e64 v1, v1, v233, s[8:9]
	v_mul_f32_e32 v0, v0, v27
	v_mul_f32_e32 v1, v1, v27
	s_mov_b64 s[2:3], exec
	s_branch .LBB1_8
.Lg_slow:
	v_cmp_lt_i32_e32 vcc, s49, v0
	s_and_saveexec_b64 s[2:3], vcc
	s_xor_b64 s[40:41], exec, s[2:3]
	s_cbranch_execz .LBB1_104
	v_lshlrev_b32_e32 v1, 2, v97
	v_and_b32_e32 v0, 4, v91
	v_and_b32_e32 v99, 4, v1
	v_mov_b32_e32 v33, v32
	v_add_u32_e32 v100, 0x9c4, v99
	v_sub_u32_e32 v101, v90, v0
	v_sub_u32_e32 v102, v83, v0
	s_mov_b32 s53, 0
	v_mov_b32_e32 v98, 0
	v_mov_b32_e32 v104, 0xff800000
	v_mov_b64_e32 v[58:59], v[32:33]
	v_mov_b64_e32 v[56:57], v[32:33]
	v_mov_b64_e32 v[52:53], v[32:33]
	v_mov_b64_e32 v[54:55], v[32:33]
	ds_write_b32 v6, v32

.LBB1_217:
	s_andn2_saveexec_b64 s[0:1], s[30:31]
	s_cbranch_execz .LBB1_384
	v_readfirstlane_b32 s34, v1
	v_readfirstlane_b32 s37, v82
	v_readfirstlane_b32 s36, v84
	v_and_b32_e32 v3, 63, v0
	v_lshlrev_b32_e32 v2, 4, v3
	s_cmp_lt_i32 s36, 0
	s_cbranch_scc1 .LBB1_384
	s_waitcnt lgkmcnt(0)
	s_and_b32 s29, s29, 0xffff
	s_mov_b32 s30, 0x17d78400
	s_mov_b32 s31, 0x20000
	s_mov_b32 s35, 0
	s_movk_i32 s7, 0x80
	s_mov_b32 s9, 0x7fffffff
	s_lshl_b32 s44, s34, 12
	s_add_u32 s44, s44, 0x4000
	s_lshl_b32 s45, s34, 10
	s_add_u32 s45, s45, 0x8000
	s_lshl_b32 s46, s34, 3
	s_add_u32 s46, s46, 0x9000
	s_and_b32 s47, s37, 1
	s_lshl_b32 s47, s47, 2
	s_mul_i32 s38, s37, 0x9c40
	s_lshl_b32 s40, s47, 4
	s_sub_u32 s38, s38, s40
	v_max_u32_e32 v12, s47, v3
	v_lshlrev_b32_e32 v12, 4, v12
	buffer_load_dwordx4 v[16:19], v12, s[28:31], s38 offen nt
	s_add_u32 s40, s38, 0x400
	buffer_load_dwordx4 v[20:23], v2, s[28:31], s40 offen nt
	s_add_u32 s40, s38, 0x800
	buffer_load_dwordx4 v[24:27], v2, s[28:31], s40 offen nt
	s_add_u32 s40, s38, 0xc00
	buffer_load_dwordx4 v[28:31], v2, s[28:31], s40 offen nt
	s_add_u32 s40, s38, 0x1000
	buffer_load_dwordx4 v[32:35], v2, s[28:31], s40 offen nt
	s_add_u32 s40, s38, 0x1400
	buffer_load_dwordx4 v[36:39], v2, s[28:31], s40 offen nt
	s_add_u32 s40, s38, 0x1800
	buffer_load_dwordx4 v[40:43], v2, s[28:31], s40 offen nt
	s_add_u32 s40, s38, 0x1c00
	buffer_load_dwordx4 v[44:47], v2, s[28:31], s40 offen nt
	s_add_u32 s40, s38, 0x2000
	buffer_load_dwordx4 v[48:51], v2, s[28:31], s40 offen nt
	s_add_u32 s40, s38, 0x2400
	buffer_load_dwordx4 v[52:55], v2, s[28:31], s40 offen nt
	s_add_u32 s40, s38, 0x2800
	buffer_load_dwordx4 v[56:59], v2, s[28:31], s40 offen nt
	s_add_u32 s40, s38, 0x2c00
	buffer_load_dwordx4 v[60:63], v2, s[28:31], s40 offen nt
	s_add_u32 s40, s38, 0x3000
	buffer_load_dwordx4 v[64:67], v2, s[28:31], s40 offen nt
	s_add_u32 s40, s38, 0x3400
	buffer_load_dwordx4 v[68:71], v2, s[28:31], s40 offen nt
	s_add_u32 s40, s38, 0x3800
	buffer_load_dwordx4 v[72:75], v2, s[28:31], s40 offen nt
	s_add_u32 s40, s38, 0x3c00
	buffer_load_dwordx4 v[76:79], v2, s[28:31], s40 offen nt
	s_add_u32 s40, s38, 0x4000
	buffer_load_dwordx4 v[80:83], v2, s[28:31], s40 offen nt
	s_add_u32 s40, s38, 0x4400
	buffer_load_dwordx4 v[84:87], v2, s[28:31], s40 offen nt
	s_add_u32 s40, s38, 0x4800
	buffer_load_dwordx4 v[88:91], v2, s[28:31], s40 offen nt
	s_add_u32 s40, s38, 0x4c00
	buffer_load_dwordx4 v[92:95], v2, s[28:31], s40 offen nt
.Lsc_row:
	v_subrev_u32_e32 v8, s47, v3
	v_lshlrev_b32_e32 v8, 2, v8
	s_add_i32 s41, s47, 3
	v_min_u32_e32 v4, s41, v3
	v_lshlrev_b32_e32 v4, 4, v4
	s_lshl_b64 s[48:49], -1, s47
	s_add_i32 s41, s47, 4
	s_lshl_b64 s[50:51], 1, s41
	s_sub_u32 s50, s50, 1
	s_and_b32 s41, s35, 1
	s_lshl_b32 s40, s41, 11
	s_add_u32 s40, s40, s44
	v_mov_b32_e32 v9, s40
	s_lshl_b32 s40, s41, 9
	s_add_u32 s40, s40, s45
	v_mov_b32_e32 v10, s40
	s_lshl_b32 s40, s41, 2
	s_add_u32 s40, s40, s46
	v_mov_b32_e32 v11, s40
	s_cmp_lt_i32 s35, s36
	s_cbranch_scc0 .Lsc_nonext
	s_add_i32 s52, s37, s33
	s_and_b32 s53, s52, 1
	s_lshl_b32 s53, s53, 2
	s_mul_i32 s39, s52, 0x9c40
	s_lshl_b32 s40, s53, 4
	s_sub_u32 s39, s39, s40
	v_max_u32_e32 v5, s53, v3
	v_lshlrev_b32_e32 v5, 4, v5
	v_mov_b32_e32 v6, v2
	s_add_i32 s40, s53, 3
	v_min_u32_e32 v7, s40, v3
	v_lshlrev_b32_e32 v7, 4, v7
	s_branch .Lsc_gotnext
.Lsc_nonext:
	s_mov_b32 s52, s37
	s_mov_b32 s53, s47
	s_mov_b32 s39, s38
	v_mov_b32_e32 v5, 0
	v_mov_b32_e32 v6, 0
	v_mov_b32_e32 v7, 0
.Lsc_gotnext:
.Lsc_wait:
	ds_read_b32 v12, v11
	s_waitcnt lgkmcnt(0)
	v_readfirstlane_b32 s42, v12
	s_cmp_eq_u32 s42, 0
	s_cbranch_scc1 .Lsc_go
	s_sleep 4
	s_branch .Lsc_wait
.Lsc_go:
	s_mov_b32 s42, 0
	s_waitcnt vmcnt(19)
	v_or3_b32 v12, v16, v17, v18
	v_bitop3_b32 v12, v12, s9, v19 bitop3:0xc8
	v_cmp_ne_u32_e32 vcc, 0, v12
	s_and_b64 vcc, vcc, s[48:49]
	s_cbranch_vccz .Lsc_s0
	s_nop 0
	v_mbcnt_lo_u32_b32 v13, vcc_lo, 0
	v_mbcnt_hi_u32_b32 v13, vcc_hi, v13
	v_add_u32_e32 v13, s42, v13
	v_cmp_gt_i32_e64 s[0:1], s7, v13
	s_and_b64 s[4:5], vcc, s[0:1]
	s_and_saveexec_b64 s[0:1], s[4:5]
	v_lshl_add_u32 v14, v13, 4, v9
	v_lshl_add_u32 v15, v13, 2, v10
	v_mov_b32_e32 v13, v8
	ds_write_b128 v14, v[16:19]
	ds_write_b32 v15, v13
	s_mov_b64 exec, -1
	s_bcnt1_i32_b64 s40, vcc
	s_add_i32 s42, s42, s40
.Lsc_s0:
	s_add_u32 s40, s38, 0x5000
	buffer_load_dwordx4 v[16:19], v2, s[28:31], s40 offen nt
	s_waitcnt vmcnt(19)
	v_or3_b32 v12, v20, v21, v22
	v_bitop3_b32 v12, v12, s9, v23 bitop3:0xc8
	v_cmp_ne_u32_e32 vcc, 0, v12
	s_cbranch_vccz .Lsc_s1
	s_nop 0
	v_mbcnt_lo_u32_b32 v13, vcc_lo, 0
	v_mbcnt_hi_u32_b32 v13, vcc_hi, v13
	v_add_u32_e32 v13, s42, v13
	v_cmp_gt_i32_e64 s[0:1], s7, v13
	s_and_b64 s[4:5], vcc, s[0:1]
	s_and_saveexec_b64 s[0:1], s[4:5]
	v_lshl_add_u32 v14, v13, 4, v9
	v_lshl_add_u32 v15, v13, 2, v10
	v_add_u32_e32 v13, 0x100, v8
	ds_write_b128 v14, v[20:23]
	ds_write_b32 v15, v13
	s_mov_b64 exec, -1
	s_bcnt1_i32_b64 s40, vcc
	s_add_i32 s42, s42, s40
.Lsc_s1:
	s_add_u32 s40, s38, 0x5400
	buffer_load_dwordx4 v[20:23], v2, s[28:31], s40 offen nt
	s_waitcnt vmcnt(19)
	v_or3_b32 v12, v24, v25, v26
	v_bitop3_b32 v12, v12, s9, v27 bitop3:0xc8
	v_cmp_ne_u32_e32 vcc, 0, v12
	s_cbranch_vccz .Lsc_s2
	s_nop 0
	v_mbcnt_lo_u32_b32 v13, vcc_lo, 0
	v_mbcnt_hi_u32_b32 v13, vcc_hi, v13
	v_add_u32_e32 v13, s42, v13
	v_cmp_gt_i32_e64 s[0:1], s7, v13
	s_and_b64 s[4:5], vcc, s[0:1]
	s_and_saveexec_b64 s[0:1], s[4:5]
	v_lshl_add_u32 v14, v13, 4, v9
	v_lshl_add_u32 v15, v13, 2, v10
	v_add_u32_e32 v13, 0x200, v8
	ds_write_b128 v14, v[24:27]
	ds_write_b32 v15, v13
	s_mov_b64 exec, -1
	s_bcnt1_i32_b64 s40, vcc
	s_add_i32 s42, s42, s40
.Lsc_s2:
	s_add_u32 s40, s38, 0x5800
	buffer_load_dwordx4 v[24:27], v2, s[28:31], s40 offen nt
	s_waitcnt vmcnt(19)
	v_or3_b32 v12, v28, v29, v30
	v_bitop3_b32 v12, v12, s9, v31 bitop3:0xc8
	v_cmp_ne_u32_e32 vcc, 0, v12
	s_cbranch_vccz .Lsc_s3
	s_nop 0
	v_mbcnt_lo_u32_b32 v13, vcc_lo, 0
	v_mbcnt_hi_u32_b32 v13, vcc_hi, v13
	v_add_u32_e32 v13, s42, v13
	v_cmp_gt_i32_e64 s[0:1], s7, v13
	s_and_b64 s[4:5], vcc, s[0:1]
	s_and_saveexec_b64 s[0:1], s[4:5]
	v_lshl_add_u32 v14, v13, 4, v9
	v_lshl_add_u32 v15, v13, 2, v10
	v_add_u32_e32 v13, 0x300, v8
	ds_write_b128 v14, v[28:31]
	ds_write_b32 v15, v13
	s_mov_b64 exec, -1
	s_bcnt1_i32_b64 s40, vcc
	s_add_i32 s42, s42, s40
.Lsc_s3:
	s_add_u32 s40, s38, 0x5c00
	buffer_load_dwordx4 v[28:31], v2, s[28:31], s40 offen nt
	s_waitcnt vmcnt(19)
	v_or3_b32 v12, v32, v33, v34
	v_bitop3_b32 v12, v12, s9, v35 bitop3:0xc8
	v_cmp_ne_u32_e32 vcc, 0, v12
	s_cbranch_vccz .Lsc_s4
	s_nop 0
	v_mbcnt_lo_u32_b32 v13, vcc_lo, 0
	v_mbcnt_hi_u32_b32 v13, vcc_hi, v13
	v_add_u32_e32 v13, s42, v13
	v_cmp_gt_i32_e64 s[0:1], s7, v13
	s_and_b64 s[4:5], vcc, s[0:1]
	s_and_saveexec_b64 s[0:1], s[4:5]
	v_lshl_add_u32 v14, v13, 4, v9
	v_lshl_add_u32 v15, v13, 2, v10
	v_add_u32_e32 v13, 0x400, v8
	ds_write_b128 v14, v[32:35]
	ds_write_b32 v15, v13
	s_mov_b64 exec, -1
	s_bcnt1_i32_b64 s40, vcc
	s_add_i32 s42, s42, s40
.Lsc_s4:
	s_add_u32 s40, s38, 0x6000
	buffer_load_dwordx4 v[32:35], v2, s[28:31], s40 offen nt
	s_waitcnt vmcnt(19)
	v_or3_b32 v12, v36, v37, v38
	v_bitop3_b32 v12, v12, s9, v39 bitop3:0xc8
	v_cmp_ne_u32_e32 vcc, 0, v12
	s_cbranch_vccz .Lsc_s5
	s_nop 0
	v_mbcnt_lo_u32_b32 v13, vcc_lo, 0
	v_mbcnt_hi_u32_b32 v13, vcc_hi, v13
	v_add_u32_e32 v13, s42, v13
	v_cmp_gt_i32_e64 s[0:1], s7, v13
	s_and_b64 s[4:5], vcc, s[0:1]
	s_and_saveexec_b64 s[0:1], s[4:5]
	v_lshl_add_u32 v14, v13, 4, v9
	v_lshl_add_u32 v15, v13, 2, v10
	v_add_u32_e32 v13, 0x500, v8
	ds_write_b128 v14, v[36:39]
	ds_write_b32 v15, v13
	s_mov_b64 exec, -1
	s_bcnt1_i32_b64 s40, vcc
	s_add_i32 s42, s42, s40
.Lsc_s5:
	s_add_u32 s40, s38, 0x6400
	buffer_load_dwordx4 v[36:39], v2, s[28:31], s40 offen nt
	s_waitcnt vmcnt(19)
	v_or3_b32 v12, v40, v41, v42
	v_bitop3_b32 v12, v12, s9, v43 bitop3:0xc8
	v_cmp_ne_u32_e32 vcc, 0, v12
	s_cbranch_vccz .Lsc_s6
	s_nop 0
	v_mbcnt_lo_u32_b32 v13, vcc_lo, 0
	v_mbcnt_hi_u32_b32 v13, vcc_hi, v13
	v_add_u32_e32 v13, s42, v13
	v_cmp_gt_i32_e64 s[0:1], s7, v13
	s_and_b64 s[4:5], vcc, s[0:1]
	s_and_saveexec_b64 s[0:1], s[4:5]
	v_lshl_add_u32 v14, v13, 4, v9
	v_lshl_add_u32 v15, v13, 2, v10
	v_add_u32_e32 v13, 0x600, v8
	ds_write_b128 v14, v[40:43]
	ds_write_b32 v15, v13
	s_mov_b64 exec, -1
	s_bcnt1_i32_b64 s40, vcc
	s_add_i32 s42, s42, s40
.Lsc_s6:
	s_add_u32 s40, s38, 0x6800
	buffer_load_dwordx4 v[40:43], v2, s[28:31], s40 offen nt
	s_waitcnt vmcnt(19)
	v_or3_b32 v12, v44, v45, v46
	v_bitop3_b32 v12, v12, s9, v47 bitop3:0xc8
	v_cmp_ne_u32_e32 vcc, 0, v12
	s_cbranch_vccz .Lsc_s7
	s_nop 0
	v_mbcnt_lo_u32_b32 v13, vcc_lo, 0
	v_mbcnt_hi_u32_b32 v13, vcc_hi, v13
	v_add_u32_e32 v13, s42, v13
	v_cmp_gt_i32_e64 s[0:1], s7, v13
	s_and_b64 s[4:5], vcc, s[0:1]
	s_and_saveexec_b64 s[0:1], s[4:5]
	v_lshl_add_u32 v14, v13, 4, v9
	v_lshl_add_u32 v15, v13, 2, v10
	v_add_u32_e32 v13, 0x700, v8
	ds_write_b128 v14, v[44:47]
	ds_write_b32 v15, v13
	s_mov_b64 exec, -1
	s_bcnt1_i32_b64 s40, vcc
	s_add_i32 s42, s42, s40
.Lsc_s7:
	s_add_u32 s40, s38, 0x6c00
	buffer_load_dwordx4 v[44:47], v2, s[28:31], s40 offen nt
	s_waitcnt vmcnt(19)
	v_or3_b32 v12, v48, v49, v50
	v_bitop3_b32 v12, v12, s9, v51 bitop3:0xc8
	v_cmp_ne_u32_e32 vcc, 0, v12
	s_cbranch_vccz .Lsc_s8
	s_nop 0
	v_mbcnt_lo_u32_b32 v13, vcc_lo, 0
	v_mbcnt_hi_u32_b32 v13, vcc_hi, v13
	v_add_u32_e32 v13, s42, v13
	v_cmp_gt_i32_e64 s[0:1], s7, v13
	s_and_b64 s[4:5], vcc, s[0:1]
	s_and_saveexec_b64 s[0:1], s[4:5]
	v_lshl_add_u32 v14, v13, 4, v9
	v_lshl_add_u32 v15, v13, 2, v10
	v_add_u32_e32 v13, 0x800, v8
	ds_write_b128 v14, v[48:51]
	ds_write_b32 v15, v13
	s_mov_b64 exec, -1
	s_bcnt1_i32_b64 s40, vcc
	s_add_i32 s42, s42, s40
.Lsc_s8:
	s_add_u32 s40, s38, 0x7000
	buffer_load_dwordx4 v[48:51], v2, s[28:31], s40 offen nt
	s_waitcnt vmcnt(19)
	v_or3_b32 v12, v52, v53, v54
	v_bitop3_b32 v12, v12, s9, v55 bitop3:0xc8
	v_cmp_ne_u32_e32 vcc, 0, v12
	s_cbranch_vccz .Lsc_s9
	s_nop 0
	v_mbcnt_lo_u32_b32 v13, vcc_lo, 0
	v_mbcnt_hi_u32_b32 v13, vcc_hi, v13
	v_add_u32_e32 v13, s42, v13
	v_cmp_gt_i32_e64 s[0:1], s7, v13
	s_and_b64 s[4:5], vcc, s[0:1]
	s_and_saveexec_b64 s[0:1], s[4:5]
	v_lshl_add_u32 v14, v13, 4, v9
	v_lshl_add_u32 v15, v13, 2, v10
	v_add_u32_e32 v13, 0x900, v8
	ds_write_b128 v14, v[52:55]
	ds_write_b32 v15, v13
	s_mov_b64 exec, -1
	s_bcnt1_i32_b64 s40, vcc
	s_add_i32 s42, s42, s40
.Lsc_s9:
	s_add_u32 s40, s38, 0x7400
	buffer_load_dwordx4 v[52:55], v2, s[28:31], s40 offen nt
	s_waitcnt vmcnt(19)
	v_or3_b32 v12, v56, v57, v58
	v_bitop3_b32 v12, v12, s9, v59 bitop3:0xc8
	v_cmp_ne_u32_e32 vcc, 0, v12
	s_cbranch_vccz .Lsc_s10
	s_nop 0
	v_mbcnt_lo_u32_b32 v13, vcc_lo, 0
	v_mbcnt_hi_u32_b32 v13, vcc_hi, v13
	v_add_u32_e32 v13, s42, v13
	v_cmp_gt_i32_e64 s[0:1], s7, v13
	s_and_b64 s[4:5], vcc, s[0:1]
	s_and_saveexec_b64 s[0:1], s[4:5]
	v_lshl_add_u32 v14, v13, 4, v9
	v_lshl_add_u32 v15, v13, 2, v10
	v_add_u32_e32 v13, 0xa00, v8
	ds_write_b128 v14, v[56:59]
	ds_write_b32 v15, v13
	s_mov_b64 exec, -1
	s_bcnt1_i32_b64 s40, vcc
	s_add_i32 s42, s42, s40
.Lsc_s10:
	s_add_u32 s40, s38, 0x7800
	buffer_load_dwordx4 v[56:59], v2, s[28:31], s40 offen nt
	s_waitcnt vmcnt(19)
	v_or3_b32 v12, v60, v61, v62
	v_bitop3_b32 v12, v12, s9, v63 bitop3:0xc8
	v_cmp_ne_u32_e32 vcc, 0, v12
	s_cbranch_vccz .Lsc_s11
	s_nop 0
	v_mbcnt_lo_u32_b32 v13, vcc_lo, 0
	v_mbcnt_hi_u32_b32 v13, vcc_hi, v13
	v_add_u32_e32 v13, s42, v13
	v_cmp_gt_i32_e64 s[0:1], s7, v13
	s_and_b64 s[4:5], vcc, s[0:1]
	s_and_saveexec_b64 s[0:1], s[4:5]
	v_lshl_add_u32 v14, v13, 4, v9
	v_lshl_add_u32 v15, v13, 2, v10
	v_add_u32_e32 v13, 0xb00, v8
	ds_write_b128 v14, v[60:63]
	ds_write_b32 v15, v13
	s_mov_b64 exec, -1
	s_bcnt1_i32_b64 s40, vcc
	s_add_i32 s42, s42, s40
.Lsc_s11:
	s_add_u32 s40, s38, 0x7c00
	buffer_load_dwordx4 v[60:63], v2, s[28:31], s40 offen nt
	s_waitcnt vmcnt(19)
	v_or3_b32 v12, v64, v65, v66
	v_bitop3_b32 v12, v12, s9, v67 bitop3:0xc8
	v_cmp_ne_u32_e32 vcc, 0, v12
	s_cbranch_vccz .Lsc_s12
	s_nop 0
	v_mbcnt_lo_u32_b32 v13, vcc_lo, 0
	v_mbcnt_hi_u32_b32 v13, vcc_hi, v13
	v_add_u32_e32 v13, s42, v13
	v_cmp_gt_i32_e64 s[0:1], s7, v13
	s_and_b64 s[4:5], vcc, s[0:1]
	s_and_saveexec_b64 s[0:1], s[4:5]
	v_lshl_add_u32 v14, v13, 4, v9
	v_lshl_add_u32 v15, v13, 2, v10
	v_add_u32_e32 v13, 0xc00, v8
	ds_write_b128 v14, v[64:67]
	ds_write_b32 v15, v13
	s_mov_b64 exec, -1
	s_bcnt1_i32_b64 s40, vcc
	s_add_i32 s42, s42, s40
.Lsc_s12:
	s_add_u32 s40, s38, 0x8000
	buffer_load_dwordx4 v[64:67], v2, s[28:31], s40 offen nt
	s_waitcnt vmcnt(19)
	v_or3_b32 v12, v68, v69, v70
	v_bitop3_b32 v12, v12, s9, v71 bitop3:0xc8
	v_cmp_ne_u32_e32 vcc, 0, v12
	s_cbranch_vccz .Lsc_s13
	s_nop 0
	v_mbcnt_lo_u32_b32 v13, vcc_lo, 0
	v_mbcnt_hi_u32_b32 v13, vcc_hi, v13
	v_add_u32_e32 v13, s42, v13
	v_cmp_gt_i32_e64 s[0:1], s7, v13
	s_and_b64 s[4:5], vcc, s[0:1]
	s_and_saveexec_b64 s[0:1], s[4:5]
	v_lshl_add_u32 v14, v13, 4, v9
	v_lshl_add_u32 v15, v13, 2, v10
	v_add_u32_e32 v13, 0xd00, v8
	ds_write_b128 v14, v[68:71]
	ds_write_b32 v15, v13
	s_mov_b64 exec, -1
	s_bcnt1_i32_b64 s40, vcc
	s_add_i32 s42, s42, s40
.Lsc_s13:
	s_add_u32 s40, s38, 0x8400
	buffer_load_dwordx4 v[68:71], v2, s[28:31], s40 offen nt
	s_waitcnt vmcnt(19)
	v_or3_b32 v12, v72, v73, v74
	v_bitop3_b32 v12, v12, s9, v75 bitop3:0xc8
	v_cmp_ne_u32_e32 vcc, 0, v12
	s_cbranch_vccz .Lsc_s14
	s_nop 0
	v_mbcnt_lo_u32_b32 v13, vcc_lo, 0
	v_mbcnt_hi_u32_b32 v13, vcc_hi, v13
	v_add_u32_e32 v13, s42, v13
	v_cmp_gt_i32_e64 s[0:1], s7, v13
	s_and_b64 s[4:5], vcc, s[0:1]
	s_and_saveexec_b64 s[0:1], s[4:5]
	v_lshl_add_u32 v14, v13, 4, v9
	v_lshl_add_u32 v15, v13, 2, v10
	v_add_u32_e32 v13, 0xe00, v8
	ds_write_b128 v14, v[72:75]
	ds_write_b32 v15, v13
	s_mov_b64 exec, -1
	s_bcnt1_i32_b64 s40, vcc
	s_add_i32 s42, s42, s40
.Lsc_s14:
	s_add_u32 s40, s38, 0x8800
	buffer_load_dwordx4 v[72:75], v2, s[28:31], s40 offen nt
	s_waitcnt vmcnt(19)
	v_or3_b32 v12, v76, v77, v78
	v_bitop3_b32 v12, v12, s9, v79 bitop3:0xc8
	v_cmp_ne_u32_e32 vcc, 0, v12
	s_cbranch_vccz .Lsc_s15
	s_nop 0
	v_mbcnt_lo_u32_b32 v13, vcc_lo, 0
	v_mbcnt_hi_u32_b32 v13, vcc_hi, v13
	v_add_u32_e32 v13, s42, v13
	v_cmp_gt_i32_e64 s[0:1], s7, v13
	s_and_b64 s[4:5], vcc, s[0:1]
	s_and_saveexec_b64 s[0:1], s[4:5]
	v_lshl_add_u32 v14, v13, 4, v9
	v_lshl_add_u32 v15, v13, 2, v10
	v_add_u32_e32 v13, 0xf00, v8
	ds_write_b128 v14, v[76:79]
	ds_write_b32 v15, v13
	s_mov_b64 exec, -1
	s_bcnt1_i32_b64 s40, vcc
	s_add_i32 s42, s42, s40
.Lsc_s15:
	s_add_u32 s40, s38, 0x8c00
	buffer_load_dwordx4 v[76:79], v2, s[28:31], s40 offen nt
	s_waitcnt vmcnt(19)
	v_or3_b32 v12, v80, v81, v82
	v_bitop3_b32 v12, v12, s9, v83 bitop3:0xc8
	v_cmp_ne_u32_e32 vcc, 0, v12
	s_cbranch_vccz .Lsc_s16
	s_nop 0
	v_mbcnt_lo_u32_b32 v13, vcc_lo, 0
	v_mbcnt_hi_u32_b32 v13, vcc_hi, v13
	v_add_u32_e32 v13, s42, v13
	v_cmp_gt_i32_e64 s[0:1], s7, v13
	s_and_b64 s[4:5], vcc, s[0:1]
	s_and_saveexec_b64 s[0:1], s[4:5]
	v_lshl_add_u32 v14, v13, 4, v9
	v_lshl_add_u32 v15, v13, 2, v10
	v_add_u32_e32 v13, 0x1000, v8
	ds_write_b128 v14, v[80:83]
	ds_write_b32 v15, v13
	s_mov_b64 exec, -1
	s_bcnt1_i32_b64 s40, vcc
	s_add_i32 s42, s42, s40
.Lsc_s16:
	s_add_u32 s40, s38, 0x9000
	buffer_load_dwordx4 v[80:83], v2, s[28:31], s40 offen nt
	s_waitcnt vmcnt(19)
	v_or3_b32 v12, v84, v85, v86
	v_bitop3_b32 v12, v12, s9, v87 bitop3:0xc8
	v_cmp_ne_u32_e32 vcc, 0, v12
	s_cbranch_vccz .Lsc_s17
	s_nop 0
	v_mbcnt_lo_u32_b32 v13, vcc_lo, 0
	v_mbcnt_hi_u32_b32 v13, vcc_hi, v13
	v_add_u32_e32 v13, s42, v13
	v_cmp_gt_i32_e64 s[0:1], s7, v13
	s_and_b64 s[4:5], vcc, s[0:1]
	s_and_saveexec_b64 s[0:1], s[4:5]
	v_lshl_add_u32 v14, v13, 4, v9
	v_lshl_add_u32 v15, v13, 2, v10
	v_add_u32_e32 v13, 0x1100, v8
	ds_write_b128 v14, v[84:87]
	ds_write_b32 v15, v13
	s_mov_b64 exec, -1
	s_bcnt1_i32_b64 s40, vcc
	s_add_i32 s42, s42, s40
.Lsc_s17:
	s_add_u32 s40, s38, 0x9400
	buffer_load_dwordx4 v[84:87], v2, s[28:31], s40 offen nt
	s_waitcnt vmcnt(19)
	v_or3_b32 v12, v88, v89, v90
	v_bitop3_b32 v12, v12, s9, v91 bitop3:0xc8
	v_cmp_ne_u32_e32 vcc, 0, v12
	s_cbranch_vccz .Lsc_s18
	s_nop 0
	v_mbcnt_lo_u32_b32 v13, vcc_lo, 0
	v_mbcnt_hi_u32_b32 v13, vcc_hi, v13
	v_add_u32_e32 v13, s42, v13
	v_cmp_gt_i32_e64 s[0:1], s7, v13
	s_and_b64 s[4:5], vcc, s[0:1]
	s_and_saveexec_b64 s[0:1], s[4:5]
	v_lshl_add_u32 v14, v13, 4, v9
	v_lshl_add_u32 v15, v13, 2, v10
	v_add_u32_e32 v13, 0x1200, v8
	ds_write_b128 v14, v[88:91]
	ds_write_b32 v15, v13
	s_mov_b64 exec, -1
	s_bcnt1_i32_b64 s40, vcc
	s_add_i32 s42, s42, s40
.Lsc_s18:
	s_add_u32 s40, s38, 0x9800
	buffer_load_dwordx4 v[88:91], v2, s[28:31], s40 offen nt
	s_waitcnt vmcnt(19)
	v_or3_b32 v12, v92, v93, v94
	v_bitop3_b32 v12, v12, s9, v95 bitop3:0xc8
	v_cmp_ne_u32_e32 vcc, 0, v12
	s_cbranch_vccz .Lsc_s19
	s_nop 0
	v_mbcnt_lo_u32_b32 v13, vcc_lo, 0
	v_mbcnt_hi_u32_b32 v13, vcc_hi, v13
	v_add_u32_e32 v13, s42, v13
	v_cmp_gt_i32_e64 s[0:1], s7, v13
	s_and_b64 s[4:5], vcc, s[0:1]
	s_and_saveexec_b64 s[0:1], s[4:5]
	v_lshl_add_u32 v14, v13, 4, v9
	v_lshl_add_u32 v15, v13, 2, v10
	v_add_u32_e32 v13, 0x1300, v8
	ds_write_b128 v14, v[92:95]
	ds_write_b32 v15, v13
	s_mov_b64 exec, -1
	s_bcnt1_i32_b64 s40, vcc
	s_add_i32 s42, s42, s40
.Lsc_s19:
	s_add_u32 s40, s38, 0x9c00
	buffer_load_dwordx4 v[92:95], v4, s[28:31], s40 offen nt
	s_waitcnt vmcnt(19)
	v_or3_b32 v12, v16, v17, v18
	v_bitop3_b32 v12, v12, s9, v19 bitop3:0xc8
	v_cmp_ne_u32_e32 vcc, 0, v12
	s_cbranch_vccz .Lsc_s20
	s_nop 0
	v_mbcnt_lo_u32_b32 v13, vcc_lo, 0
	v_mbcnt_hi_u32_b32 v13, vcc_hi, v13
	v_add_u32_e32 v13, s42, v13
	v_cmp_gt_i32_e64 s[0:1], s7, v13
	s_and_b64 s[4:5], vcc, s[0:1]
	s_and_saveexec_b64 s[0:1], s[4:5]
	v_lshl_add_u32 v14, v13, 4, v9
	v_lshl_add_u32 v15, v13, 2, v10
	v_add_u32_e32 v13, 0x1400, v8
	ds_write_b128 v14, v[16:19]
	ds_write_b32 v15, v13
	s_mov_b64 exec, -1
	s_bcnt1_i32_b64 s40, vcc
	s_add_i32 s42, s42, s40
.Lsc_s20:
	s_mov_b32 s40, s39
	buffer_load_dwordx4 v[16:19], v5, s[28:31], s40 offen nt
	s_waitcnt vmcnt(19)
	v_or3_b32 v12, v20, v21, v22
	v_bitop3_b32 v12, v12, s9, v23 bitop3:0xc8
	v_cmp_ne_u32_e32 vcc, 0, v12
	s_cbranch_vccz .Lsc_s21
	s_nop 0
	v_mbcnt_lo_u32_b32 v13, vcc_lo, 0
	v_mbcnt_hi_u32_b32 v13, vcc_hi, v13
	v_add_u32_e32 v13, s42, v13
	v_cmp_gt_i32_e64 s[0:1], s7, v13
	s_and_b64 s[4:5], vcc, s[0:1]
	s_and_saveexec_b64 s[0:1], s[4:5]
	v_lshl_add_u32 v14, v13, 4, v9
	v_lshl_add_u32 v15, v13, 2, v10
	v_add_u32_e32 v13, 0x1500, v8
	ds_write_b128 v14, v[20:23]
	ds_write_b32 v15, v13
	s_mov_b64 exec, -1
	s_bcnt1_i32_b64 s40, vcc
	s_add_i32 s42, s42, s40
.Lsc_s21:
	s_add_u32 s40, s39, 0x400
	buffer_load_dwordx4 v[20:23], v6, s[28:31], s40 offen nt
	s_waitcnt vmcnt(19)
	v_or3_b32 v12, v24, v25, v26
	v_bitop3_b32 v12, v12, s9, v27 bitop3:0xc8
	v_cmp_ne_u32_e32 vcc, 0, v12
	s_cbranch_vccz .Lsc_s22
	s_nop 0
	v_mbcnt_lo_u32_b32 v13, vcc_lo, 0
	v_mbcnt_hi_u32_b32 v13, vcc_hi, v13
	v_add_u32_e32 v13, s42, v13
	v_cmp_gt_i32_e64 s[0:1], s7, v13
	s_and_b64 s[4:5], vcc, s[0:1]
	s_and_saveexec_b64 s[0:1], s[4:5]
	v_lshl_add_u32 v14, v13, 4, v9
	v_lshl_add_u32 v15, v13, 2, v10
	v_add_u32_e32 v13, 0x1600, v8
	ds_write_b128 v14, v[24:27]
	ds_write_b32 v15, v13
	s_mov_b64 exec, -1
	s_bcnt1_i32_b64 s40, vcc
	s_add_i32 s42, s42, s40
.Lsc_s22:
	s_add_u32 s40, s39, 0x800
	buffer_load_dwordx4 v[24:27], v6, s[28:31], s40 offen nt
	s_waitcnt vmcnt(19)
	v_or3_b32 v12, v28, v29, v30
	v_bitop3_b32 v12, v12, s9, v31 bitop3:0xc8
	v_cmp_ne_u32_e32 vcc, 0, v12
	s_cbranch_vccz .Lsc_s23
	s_nop 0
	v_mbcnt_lo_u32_b32 v13, vcc_lo, 0
	v_mbcnt_hi_u32_b32 v13, vcc_hi, v13
	v_add_u32_e32 v13, s42, v13
	v_cmp_gt_i32_e64 s[0:1], s7, v13
	s_and_b64 s[4:5], vcc, s[0:1]
	s_and_saveexec_b64 s[0:1], s[4:5]
	v_lshl_add_u32 v14, v13, 4, v9
	v_lshl_add_u32 v15, v13, 2, v10
	v_add_u32_e32 v13, 0x1700, v8
	ds_write_b128 v14, v[28:31]
	ds_write_b32 v15, v13
	s_mov_b64 exec, -1
	s_bcnt1_i32_b64 s40, vcc
	s_add_i32 s42, s42, s40
.Lsc_s23:
	s_add_u32 s40, s39, 0xc00
	buffer_load_dwordx4 v[28:31], v6, s[28:31], s40 offen nt
	s_waitcnt vmcnt(19)
	v_or3_b32 v12, v32, v33, v34
	v_bitop3_b32 v12, v12, s9, v35 bitop3:0xc8
	v_cmp_ne_u32_e32 vcc, 0, v12
	s_cbranch_vccz .Lsc_s24
	s_nop 0
	v_mbcnt_lo_u32_b32 v13, vcc_lo, 0
	v_mbcnt_hi_u32_b32 v13, vcc_hi, v13
	v_add_u32_e32 v13, s42, v13
	v_cmp_gt_i32_e64 s[0:1], s7, v13
	s_and_b64 s[4:5], vcc, s[0:1]
	s_and_saveexec_b64 s[0:1], s[4:5]
	v_lshl_add_u32 v14, v13, 4, v9
	v_lshl_add_u32 v15, v13, 2, v10
	v_add_u32_e32 v13, 0x1800, v8
	ds_write_b128 v14, v[32:35]
	ds_write_b32 v15, v13
	s_mov_b64 exec, -1
	s_bcnt1_i32_b64 s40, vcc
	s_add_i32 s42, s42, s40
.Lsc_s24:
	s_add_u32 s40, s39, 0x1000
	buffer_load_dwordx4 v[32:35], v6, s[28:31], s40 offen nt
	s_waitcnt vmcnt(19)
	v_or3_b32 v12, v36, v37, v38
	v_bitop3_b32 v12, v12, s9, v39 bitop3:0xc8
	v_cmp_ne_u32_e32 vcc, 0, v12
	s_cbranch_vccz .Lsc_s25
	s_nop 0
	v_mbcnt_lo_u32_b32 v13, vcc_lo, 0
	v_mbcnt_hi_u32_b32 v13, vcc_hi, v13
	v_add_u32_e32 v13, s42, v13
	v_cmp_gt_i32_e64 s[0:1], s7, v13
	s_and_b64 s[4:5], vcc, s[0:1]
	s_and_saveexec_b64 s[0:1], s[4:5]
	v_lshl_add_u32 v14, v13, 4, v9
	v_lshl_add_u32 v15, v13, 2, v10
	v_add_u32_e32 v13, 0x1900, v8
	ds_write_b128 v14, v[36:39]
	ds_write_b32 v15, v13
	s_mov_b64 exec, -1
	s_bcnt1_i32_b64 s40, vcc
	s_add_i32 s42, s42, s40
.Lsc_s25:
	s_add_u32 s40, s39, 0x1400
	buffer_load_dwordx4 v[36:39], v6, s[28:31], s40 offen nt
	s_waitcnt vmcnt(19)
	v_or3_b32 v12, v40, v41, v42
	v_bitop3_b32 v12, v12, s9, v43 bitop3:0xc8
	v_cmp_ne_u32_e32 vcc, 0, v12
	s_cbranch_vccz .Lsc_s26
	s_nop 0
	v_mbcnt_lo_u32_b32 v13, vcc_lo, 0
	v_mbcnt_hi_u32_b32 v13, vcc_hi, v13
	v_add_u32_e32 v13, s42, v13
	v_cmp_gt_i32_e64 s[0:1], s7, v13
	s_and_b64 s[4:5], vcc, s[0:1]
	s_and_saveexec_b64 s[0:1], s[4:5]
	v_lshl_add_u32 v14, v13, 4, v9
	v_lshl_add_u32 v15, v13, 2, v10
	v_add_u32_e32 v13, 0x1a00, v8
	ds_write_b128 v14, v[40:43]
	ds_write_b32 v15, v13
	s_mov_b64 exec, -1
	s_bcnt1_i32_b64 s40, vcc
	s_add_i32 s42, s42, s40
.Lsc_s26:
	s_add_u32 s40, s39, 0x1800
	buffer_load_dwordx4 v[40:43], v6, s[28:31], s40 offen nt
	s_waitcnt vmcnt(19)
	v_or3_b32 v12, v44, v45, v46
	v_bitop3_b32 v12, v12, s9, v47 bitop3:0xc8
	v_cmp_ne_u32_e32 vcc, 0, v12
	s_cbranch_vccz .Lsc_s27
	s_nop 0
	v_mbcnt_lo_u32_b32 v13, vcc_lo, 0
	v_mbcnt_hi_u32_b32 v13, vcc_hi, v13
	v_add_u32_e32 v13, s42, v13
	v_cmp_gt_i32_e64 s[0:1], s7, v13
	s_and_b64 s[4:5], vcc, s[0:1]
	s_and_saveexec_b64 s[0:1], s[4:5]
	v_lshl_add_u32 v14, v13, 4, v9
	v_lshl_add_u32 v15, v13, 2, v10
	v_add_u32_e32 v13, 0x1b00, v8
	ds_write_b128 v14, v[44:47]
	ds_write_b32 v15, v13
	s_mov_b64 exec, -1
	s_bcnt1_i32_b64 s40, vcc
	s_add_i32 s42, s42, s40
.Lsc_s27:
	s_add_u32 s40, s39, 0x1c00
	buffer_load_dwordx4 v[44:47], v6, s[28:31], s40 offen nt
	s_waitcnt vmcnt(19)
	v_or3_b32 v12, v48, v49, v50
	v_bitop3_b32 v12, v12, s9, v51 bitop3:0xc8
	v_cmp_ne_u32_e32 vcc, 0, v12
	s_cbranch_vccz .Lsc_s28
	s_nop 0
	v_mbcnt_lo_u32_b32 v13, vcc_lo, 0
	v_mbcnt_hi_u32_b32 v13, vcc_hi, v13
	v_add_u32_e32 v13, s42, v13
	v_cmp_gt_i32_e64 s[0:1], s7, v13
	s_and_b64 s[4:5], vcc, s[0:1]
	s_and_saveexec_b64 s[0:1], s[4:5]
	v_lshl_add_u32 v14, v13, 4, v9
	v_lshl_add_u32 v15, v13, 2, v10
	v_add_u32_e32 v13, 0x1c00, v8
	ds_write_b128 v14, v[48:51]
	ds_write_b32 v15, v13
	s_mov_b64 exec, -1
	s_bcnt1_i32_b64 s40, vcc
	s_add_i32 s42, s42, s40
.Lsc_s28:
	s_add_u32 s40, s39, 0x2000
	buffer_load_dwordx4 v[48:51], v6, s[28:31], s40 offen nt
	s_waitcnt vmcnt(19)
	v_or3_b32 v12, v52, v53, v54
	v_bitop3_b32 v12, v12, s9, v55 bitop3:0xc8
	v_cmp_ne_u32_e32 vcc, 0, v12
	s_cbranch_vccz .Lsc_s29
	s_nop 0
	v_mbcnt_lo_u32_b32 v13, vcc_lo, 0
	v_mbcnt_hi_u32_b32 v13, vcc_hi, v13
	v_add_u32_e32 v13, s42, v13
	v_cmp_gt_i32_e64 s[0:1], s7, v13
	s_and_b64 s[4:5], vcc, s[0:1]
	s_and_saveexec_b64 s[0:1], s[4:5]
	v_lshl_add_u32 v14, v13, 4, v9
	v_lshl_add_u32 v15, v13, 2, v10
	v_add_u32_e32 v13, 0x1d00, v8
	ds_write_b128 v14, v[52:55]
	ds_write_b32 v15, v13
	s_mov_b64 exec, -1
	s_bcnt1_i32_b64 s40, vcc
	s_add_i32 s42, s42, s40
.Lsc_s29:
	s_add_u32 s40, s39, 0x2400
	buffer_load_dwordx4 v[52:55], v6, s[28:31], s40 offen nt
	s_waitcnt vmcnt(19)
	v_or3_b32 v12, v56, v57, v58
	v_bitop3_b32 v12, v12, s9, v59 bitop3:0xc8
	v_cmp_ne_u32_e32 vcc, 0, v12
	s_cbranch_vccz .Lsc_s30
	s_nop 0
	v_mbcnt_lo_u32_b32 v13, vcc_lo, 0
	v_mbcnt_hi_u32_b32 v13, vcc_hi, v13
	v_add_u32_e32 v13, s42, v13
	v_cmp_gt_i32_e64 s[0:1], s7, v13
	s_and_b64 s[4:5], vcc, s[0:1]
	s_and_saveexec_b64 s[0:1], s[4:5]
	v_lshl_add_u32 v14, v13, 4, v9
	v_lshl_add_u32 v15, v13, 2, v10
	v_add_u32_e32 v13, 0x1e00, v8
	ds_write_b128 v14, v[56:59]
	ds_write_b32 v15, v13
	s_mov_b64 exec, -1
	s_bcnt1_i32_b64 s40, vcc
	s_add_i32 s42, s42, s40
.Lsc_s30:
	s_add_u32 s40, s39, 0x2800
	buffer_load_dwordx4 v[56:59], v6, s[28:31], s40 offen nt
	s_waitcnt vmcnt(19)
	v_or3_b32 v12, v60, v61, v62
	v_bitop3_b32 v12, v12, s9, v63 bitop3:0xc8
	v_cmp_ne_u32_e32 vcc, 0, v12
	s_cbranch_vccz .Lsc_s31
	s_nop 0
	v_mbcnt_lo_u32_b32 v13, vcc_lo, 0
	v_mbcnt_hi_u32_b32 v13, vcc_hi, v13
	v_add_u32_e32 v13, s42, v13
	v_cmp_gt_i32_e64 s[0:1], s7, v13
	s_and_b64 s[4:5], vcc, s[0:1]
	s_and_saveexec_b64 s[0:1], s[4:5]
	v_lshl_add_u32 v14, v13, 4, v9
	v_lshl_add_u32 v15, v13, 2, v10
	v_add_u32_e32 v13, 0x1f00, v8
	ds_write_b128 v14, v[60:63]
	ds_write_b32 v15, v13
	s_mov_b64 exec, -1
	s_bcnt1_i32_b64 s40, vcc
	s_add_i32 s42, s42, s40
.Lsc_s31:
	s_add_u32 s40, s39, 0x2c00
	buffer_load_dwordx4 v[60:63], v6, s[28:31], s40 offen nt
	s_waitcnt vmcnt(19)
	v_or3_b32 v12, v64, v65, v66
	v_bitop3_b32 v12, v12, s9, v67 bitop3:0xc8
	v_cmp_ne_u32_e32 vcc, 0, v12
	s_cbranch_vccz .Lsc_s32
	s_nop 0
	v_mbcnt_lo_u32_b32 v13, vcc_lo, 0
	v_mbcnt_hi_u32_b32 v13, vcc_hi, v13
	v_add_u32_e32 v13, s42, v13
	v_cmp_gt_i32_e64 s[0:1], s7, v13
	s_and_b64 s[4:5], vcc, s[0:1]
	s_and_saveexec_b64 s[0:1], s[4:5]
	v_lshl_add_u32 v14, v13, 4, v9
	v_lshl_add_u32 v15, v13, 2, v10
	v_add_u32_e32 v13, 0x2000, v8
	ds_write_b128 v14, v[64:67]
	ds_write_b32 v15, v13
	s_mov_b64 exec, -1
	s_bcnt1_i32_b64 s40, vcc
	s_add_i32 s42, s42, s40
.Lsc_s32:
	s_add_u32 s40, s39, 0x3000
	buffer_load_dwordx4 v[64:67], v6, s[28:31], s40 offen nt
	s_waitcnt vmcnt(19)
	v_or3_b32 v12, v68, v69, v70
	v_bitop3_b32 v12, v12, s9, v71 bitop3:0xc8
	v_cmp_ne_u32_e32 vcc, 0, v12
	s_cbranch_vccz .Lsc_s33
	s_nop 0
	v_mbcnt_lo_u32_b32 v13, vcc_lo, 0
	v_mbcnt_hi_u32_b32 v13, vcc_hi, v13
	v_add_u32_e32 v13, s42, v13
	v_cmp_gt_i32_e64 s[0:1], s7, v13
	s_and_b64 s[4:5], vcc, s[0:1]
	s_and_saveexec_b64 s[0:1], s[4:5]
	v_lshl_add_u32 v14, v13, 4, v9
	v_lshl_add_u32 v15, v13, 2, v10
	v_add_u32_e32 v13, 0x2100, v8
	ds_write_b128 v14, v[68:71]
	ds_write_b32 v15, v13
	s_mov_b64 exec, -1
	s_bcnt1_i32_b64 s40, vcc
	s_add_i32 s42, s42, s40
.Lsc_s33:
	s_add_u32 s40, s39, 0x3400
	buffer_load_dwordx4 v[68:71], v6, s[28:31], s40 offen nt
	s_waitcnt vmcnt(19)
	v_or3_b32 v12, v72, v73, v74
	v_bitop3_b32 v12, v12, s9, v75 bitop3:0xc8
	v_cmp_ne_u32_e32 vcc, 0, v12
	s_cbranch_vccz .Lsc_s34
	s_nop 0
	v_mbcnt_lo_u32_b32 v13, vcc_lo, 0
	v_mbcnt_hi_u32_b32 v13, vcc_hi, v13
	v_add_u32_e32 v13, s42, v13
	v_cmp_gt_i32_e64 s[0:1], s7, v13
	s_and_b64 s[4:5], vcc, s[0:1]
	s_and_saveexec_b64 s[0:1], s[4:5]
	v_lshl_add_u32 v14, v13, 4, v9
	v_lshl_add_u32 v15, v13, 2, v10
	v_add_u32_e32 v13, 0x2200, v8
	ds_write_b128 v14, v[72:75]
	ds_write_b32 v15, v13
	s_mov_b64 exec, -1
	s_bcnt1_i32_b64 s40, vcc
	s_add_i32 s42, s42, s40
.Lsc_s34:
	s_add_u32 s40, s39, 0x3800
	buffer_load_dwordx4 v[72:75], v6, s[28:31], s40 offen nt
	s_waitcnt vmcnt(19)
	v_or3_b32 v12, v76, v77, v78
	v_bitop3_b32 v12, v12, s9, v79 bitop3:0xc8
	v_cmp_ne_u32_e32 vcc, 0, v12
	s_cbranch_vccz .Lsc_s35
	s_nop 0
	v_mbcnt_lo_u32_b32 v13, vcc_lo, 0
	v_mbcnt_hi_u32_b32 v13, vcc_hi, v13
	v_add_u32_e32 v13, s42, v13
	v_cmp_gt_i32_e64 s[0:1], s7, v13
	s_and_b64 s[4:5], vcc, s[0:1]
	s_and_saveexec_b64 s[0:1], s[4:5]
	v_lshl_add_u32 v14, v13, 4, v9
	v_lshl_add_u32 v15, v13, 2, v10
	v_add_u32_e32 v13, 0x2300, v8
	ds_write_b128 v14, v[76:79]
	ds_write_b32 v15, v13
	s_mov_b64 exec, -1
	s_bcnt1_i32_b64 s40, vcc
	s_add_i32 s42, s42, s40
.Lsc_s35:
	s_add_u32 s40, s39, 0x3c00
	buffer_load_dwordx4 v[76:79], v6, s[28:31], s40 offen nt
	s_waitcnt vmcnt(19)
	v_or3_b32 v12, v80, v81, v82
	v_bitop3_b32 v12, v12, s9, v83 bitop3:0xc8
	v_cmp_ne_u32_e32 vcc, 0, v12
	s_cbranch_vccz .Lsc_s36
	s_nop 0
	v_mbcnt_lo_u32_b32 v13, vcc_lo, 0
	v_mbcnt_hi_u32_b32 v13, vcc_hi, v13
	v_add_u32_e32 v13, s42, v13
	v_cmp_gt_i32_e64 s[0:1], s7, v13
	s_and_b64 s[4:5], vcc, s[0:1]
	s_and_saveexec_b64 s[0:1], s[4:5]
	v_lshl_add_u32 v14, v13, 4, v9
	v_lshl_add_u32 v15, v13, 2, v10
	v_add_u32_e32 v13, 0x2400, v8
	ds_write_b128 v14, v[80:83]
	ds_write_b32 v15, v13
	s_mov_b64 exec, -1
	s_bcnt1_i32_b64 s40, vcc
	s_add_i32 s42, s42, s40
.Lsc_s36:
	s_add_u32 s40, s39, 0x4000
	buffer_load_dwordx4 v[80:83], v6, s[28:31], s40 offen nt
	s_waitcnt vmcnt(19)
	v_or3_b32 v12, v84, v85, v86
	v_bitop3_b32 v12, v12, s9, v87 bitop3:0xc8
	v_cmp_ne_u32_e32 vcc, 0, v12
	s_cbranch_vccz .Lsc_s37
	s_nop 0
	v_mbcnt_lo_u32_b32 v13, vcc_lo, 0
	v_mbcnt_hi_u32_b32 v13, vcc_hi, v13
	v_add_u32_e32 v13, s42, v13
	v_cmp_gt_i32_e64 s[0:1], s7, v13
	s_and_b64 s[4:5], vcc, s[0:1]
	s_and_saveexec_b64 s[0:1], s[4:5]
	v_lshl_add_u32 v14, v13, 4, v9
	v_lshl_add_u32 v15, v13, 2, v10
	v_add_u32_e32 v13, 0x2500, v8
	ds_write_b128 v14, v[84:87]
	ds_write_b32 v15, v13
	s_mov_b64 exec, -1
	s_bcnt1_i32_b64 s40, vcc
	s_add_i32 s42, s42, s40
.Lsc_s37:
	s_add_u32 s40, s39, 0x4400
	buffer_load_dwordx4 v[84:87], v6, s[28:31], s40 offen nt
	s_waitcnt vmcnt(19)
	v_or3_b32 v12, v88, v89, v90
	v_bitop3_b32 v12, v12, s9, v91 bitop3:0xc8
	v_cmp_ne_u32_e32 vcc, 0, v12
	s_cbranch_vccz .Lsc_s38
	s_nop 0
	v_mbcnt_lo_u32_b32 v13, vcc_lo, 0
	v_mbcnt_hi_u32_b32 v13, vcc_hi, v13
	v_add_u32_e32 v13, s42, v13
	v_cmp_gt_i32_e64 s[0:1], s7, v13
	s_and_b64 s[4:5], vcc, s[0:1]
	s_and_saveexec_b64 s[0:1], s[4:5]
	v_lshl_add_u32 v14, v13, 4, v9
	v_lshl_add_u32 v15, v13, 2, v10
	v_add_u32_e32 v13, 0x2600, v8
	ds_write_b128 v14, v[88:91]
	ds_write_b32 v15, v13
	s_mov_b64 exec, -1
	s_bcnt1_i32_b64 s40, vcc
	s_add_i32 s42, s42, s40
.Lsc_s38:
	s_add_u32 s40, s39, 0x4800
	buffer_load_dwordx4 v[88:91], v6, s[28:31], s40 offen nt
	s_waitcnt vmcnt(19)
	v_or3_b32 v12, v92, v93, v94
	v_bitop3_b32 v12, v12, s9, v95 bitop3:0xc8
	v_cmp_ne_u32_e32 vcc, 0, v12
	s_and_b64 vcc, vcc, s[50:51]
	s_cbranch_vccz .Lsc_s39
	s_nop 0
	v_mbcnt_lo_u32_b32 v13, vcc_lo, 0
	v_mbcnt_hi_u32_b32 v13, vcc_hi, v13
	v_add_u32_e32 v13, s42, v13
	v_cmp_gt_i32_e64 s[0:1], s7, v13
	s_and_b64 s[4:5], vcc, s[0:1]
	s_and_saveexec_b64 s[0:1], s[4:5]
	v_lshl_add_u32 v14, v13, 4, v9
	v_lshl_add_u32 v15, v13, 2, v10
	v_add_u32_e32 v13, 0x2700, v8
	ds_write_b128 v14, v[92:95]
	ds_write_b32 v15, v13
	s_mov_b64 exec, -1
	s_bcnt1_i32_b64 s40, vcc
	s_add_i32 s42, s42, s40
.Lsc_s39:
	s_add_u32 s40, s39, 0x4c00
	buffer_load_dwordx4 v[92:95], v6, s[28:31], s40 offen nt
	s_waitcnt lgkmcnt(0)
	s_add_i32 s42, s42, 1
	v_mov_b32_e32 v12, s42
	ds_write_b32 v11, v12
	s_cmp_eq_u32 s35, s36
	s_cbranch_scc1 .LBB1_384
	s_add_i32 s35, s35, 1
	s_mov_b32 s37, s52
	s_mov_b32 s38, s39
	s_mov_b32 s47, s53
	s_branch .Lsc_row

	.amdhsa_kernel _Z11attn_kernelPKfS0_PKDv8_DF16_S0_Pfi
		.amdhsa_group_segment_fixed_size 36896
		.amdhsa_private_segment_fixed_size 0
		.amdhsa_kernarg_size 44
		.amdhsa_user_sgpr_count 2
		.amdhsa_user_sgpr_dispatch_ptr 0
		.amdhsa_user_sgpr_queue_ptr 0
		.amdhsa_user_sgpr_kernarg_segment_ptr 1
		.amdhsa_user_sgpr_dispatch_id 0
		.amdhsa_user_sgpr_kernarg_preload_length 0
		.amdhsa_user_sgpr_kernarg_preload_offset 0
		.amdhsa_user_sgpr_private_segment_size 0
		.amdhsa_uses_dynamic_stack 0
		.amdhsa_enable_private_segment 0
		.amdhsa_system_sgpr_workgroup_id_x 1
		.amdhsa_system_sgpr_workgroup_id_y 0
		.amdhsa_system_sgpr_workgroup_id_z 0
		.amdhsa_system_sgpr_workgroup_info 0
		.amdhsa_system_vgpr_workitem_id 0
		.amdhsa_next_free_vgpr 248
		.amdhsa_next_free_sgpr 54
		.amdhsa_accum_offset 248
		.amdhsa_reserve_vcc 1
		.amdhsa_float_round_mode_32 0
		.amdhsa_float_round_mode_16_64 0
		.amdhsa_float_denorm_mode_32 3
		.amdhsa_float_denorm_mode_16_64 3
		.amdhsa_dx10_clamp 1
		.amdhsa_ieee_mode 1
		.amdhsa_fp16_overflow 0
		.amdhsa_tg_split 0
		.amdhsa_exception_fp_ieee_invalid_op 0
		.amdhsa_exception_fp_denorm_src 0
		.amdhsa_exception_fp_ieee_div_zero 0
		.amdhsa_exception_fp_ieee_overflow 0
		.amdhsa_exception_fp_ieee_underflow 0
		.amdhsa_exception_fp_ieee_inexact 0
		.amdhsa_exception_int_div_zero 0
	.end_amdhsa_kernel

.Lfunc_end1:
	.size	_Z11attn_kernelPKfS0_PKDv8_DF16_S0_Pfi, .Lfunc_end1-_Z11attn_kernelPKfS0_PKDv8_DF16_S0_Pfi
	.set _Z11attn_kernelPKfS0_PKDv8_DF16_S0_Pfi.num_vgpr, 248
	.set _Z11attn_kernelPKfS0_PKDv8_DF16_S0_Pfi.num_agpr, 0
	.set _Z11attn_kernelPKfS0_PKDv8_DF16_S0_Pfi.numbered_sgpr, 54
	.set _Z11attn_kernelPKfS0_PKDv8_DF16_S0_Pfi.num_named_barrier, 0
	.set _Z11attn_kernelPKfS0_PKDv8_DF16_S0_Pfi.private_seg_size, 0
	.set _Z11attn_kernelPKfS0_PKDv8_DF16_S0_Pfi.uses_vcc, 1
	.set _Z11attn_kernelPKfS0_PKDv8_DF16_S0_Pfi.uses_flat_scratch, 0
	.set _Z11attn_kernelPKfS0_PKDv8_DF16_S0_Pfi.has_dyn_sized_stack, 0
	.set _Z11attn_kernelPKfS0_PKDv8_DF16_S0_Pfi.has_recursion, 0
	.set _Z11attn_kernelPKfS0_PKDv8_DF16_S0_Pfi.has_indirect_call, 0

amdhsa.kernels:
  - .agpr_count:     0
    .args:
      - .actual_access:  read_only
        .address_space:  global
        .offset:         0
        .size:           8
        .value_kind:     global_buffer
      - .actual_access:  read_only
        .address_space:  global
        .offset:         8
        .size:           8
        .value_kind:     global_buffer
      - .actual_access:  write_only
        .address_space:  global
        .offset:         16
        .size:           8
        .value_kind:     global_buffer
      - .actual_access:  write_only
        .address_space:  global
        .offset:         24
        .size:           8
        .value_kind:     global_buffer
      - .offset:         32
        .size:           4
        .value_kind:     hidden_block_count_x
      - .offset:         36
        .size:           4
        .value_kind:     hidden_block_count_y
      - .offset:         40
        .size:           4
        .value_kind:     hidden_block_count_z
      - .offset:         44
        .size:           2
        .value_kind:     hidden_group_size_x
      - .offset:         46
        .size:           2
        .value_kind:     hidden_group_size_y
      - .offset:         48
        .size:           2
        .value_kind:     hidden_group_size_z
      - .offset:         50
        .size:           2
        .value_kind:     hidden_remainder_x
      - .offset:         52
        .size:           2
        .value_kind:     hidden_remainder_y
      - .offset:         54
        .size:           2
        .value_kind:     hidden_remainder_z
      - .offset:         72
        .size:           8
        .value_kind:     hidden_global_offset_x
      - .offset:         80
        .size:           8
        .value_kind:     hidden_global_offset_y
      - .offset:         88
        .size:           8
        .value_kind:     hidden_global_offset_z
      - .offset:         96
        .size:           2
        .value_kind:     hidden_grid_dims
    .group_segment_fixed_size: 0
    .kernarg_segment_align: 8
    .kernarg_segment_size: 288
    .language:       OpenCL C
    .language_version:
      - 2
      - 0
    .max_flat_workgroup_size: 256
    .name:           _Z11prep_kernelPKfS0_PfPDv4_DF16_
    .private_segment_fixed_size: 0
    .sgpr_count:     14
    .sgpr_spill_count: 0
    .symbol:         _Z11prep_kernelPKfS0_PfPDv4_DF16_.kd
    .uniform_work_group_size: 1
    .uses_dynamic_stack: false
    .vgpr_count:     17
    .vgpr_spill_count: 0
    .wavefront_size: 64
  - .agpr_count:     0
    .args:
      - .actual_access:  read_only
        .address_space:  global
        .offset:         0
        .size:           8
        .value_kind:     global_buffer
      - .actual_access:  read_only
        .address_space:  global
        .offset:         8
        .size:           8
        .value_kind:     global_buffer
      - .actual_access:  read_only
        .address_space:  global
        .offset:         16
        .size:           8
        .value_kind:     global_buffer
      - .actual_access:  read_only
        .address_space:  global
        .offset:         24
        .size:           8
        .value_kind:     global_buffer
      - .actual_access:  write_only
        .address_space:  global
        .offset:         32
        .size:           8
        .value_kind:     global_buffer
      - .offset:         40
        .size:           4
        .value_kind:     by_value
    .group_segment_fixed_size: 36896
    .kernarg_segment_align: 8
    .kernarg_segment_size: 44
    .language:       OpenCL C
    .language_version:
      - 2
      - 0
    .max_flat_workgroup_size: 512
    .name:           _Z11attn_kernelPKfS0_PKDv8_DF16_S0_Pfi
    .private_segment_fixed_size: 0
    .sgpr_count:     60
    .sgpr_spill_count: 0
    .symbol:         _Z11attn_kernelPKfS0_PKDv8_DF16_S0_Pfi.kd
    .uniform_work_group_size: 1
    .uses_dynamic_stack: false
    .vgpr_count:     248
    .vgpr_spill_count: 0
    .wavefront_size: 64
